# scan2 block loop waits above stores; dispatch expert counts read with 8 wide loads instead of 32 serial round trips
# speedup vs baseline: 1.0197x; 1.0008x over previous
.LBB0_651:
	s_lshr_b32 s14, s39, 3
	s_mul_i32 s14, s14, 0x8800
	s_ashr_i32 s15, s14, 31
	s_lshl_b64 s[14:15], s[14:15], 11
	s_add_u32 s16, s21, s14
	s_addc_u32 s17, s22, s15
	s_add_u32 s18, s23, s14
	s_addc_u32 s19, s24, s15
	s_add_u32 s14, s25, s14
	s_addc_u32 s15, s26, s15
	s_and_b64 s[42:43], s[12:13], exec
	s_cselect_b32 s37, s28, 0xfffff800
	v_lshl_or_b32 v1, s40, 11, v59
	v_add_u32_e32 v6, s37, v1
	global_load_dwordx2 v[48:49], v1, s[16:17]
	global_load_dwordx2 v[44:45], v1, s[18:19]
	global_load_dwordx2 v[36:37], v6, s[16:17]
	global_load_dwordx2 v[30:31], v6, s[18:19]
	v_add_u32_e32 v1, s37, v6
	v_add_u32_e32 v6, s37, v1
	global_load_dwordx2 v[28:29], v1, s[16:17]
	global_load_dwordx2 v[26:27], v1, s[18:19]
	global_load_dwordx2 v[24:25], v6, s[16:17]
	global_load_dwordx2 v[22:23], v6, s[18:19]
	v_add_u32_e32 v1, s37, v6
	v_add_u32_e32 v6, s37, v1
	global_load_dwordx2 v[20:21], v1, s[16:17]
	global_load_dwordx2 v[18:19], v1, s[18:19]
	global_load_dwordx2 v[16:17], v6, s[16:17]
	global_load_dwordx2 v[14:15], v6, s[18:19]
	v_add_u32_e32 v1, s37, v6
	v_add_u32_e32 v6, s37, v1
	global_load_dwordx2 v[12:13], v1, s[16:17]
	global_load_dwordx2 v[10:11], v1, s[18:19]
	global_load_dwordx2 v[8:9], v6, s[16:17]
	s_nop 0
	global_load_dwordx2 v[6:7], v6, s[18:19]
	s_mulk_i32 s39, 0x1100
	s_mulk_i32 s38, 0x88
	s_sub_i32 s38, s39, s38
	s_mov_b32 s39, 0
	s_waitcnt vmcnt(0)
.LBB0_652:
	s_add_i32 s42, s34, s39
	s_add_i32 s40, s42, 0xffffff00
	s_cmpk_lt_i32 s42, 0x100
	s_cselect_b32 s41, 0xff, s27
	s_cselect_b32 s43, s42, s40
	s_cselect_b32 s44, s36, s35
	s_add_i32 s45, s41, s38
	s_and_b64 s[40:41], s[12:13], exec
	s_cselect_b32 s40, s43, s45
	s_add_i32 s41, s42, 8
	s_addk_i32 s42, 0xff08
	s_add_i32 s43, s40, s44
	s_cmpk_lt_i32 s41, 0x100
	s_cselect_b32 s40, 0xff, s27
	s_cselect_b32 s42, s41, s42
	s_cselect_b32 s44, s36, s35
	s_add_i32 s38, s38, -8
	s_add_i32 s45, s38, s40
	s_and_b64 s[40:41], s[12:13], exec
	s_waitcnt vmcnt(8)
	v_lshlrev_b32_e32 v1, 16, v48
	s_cselect_b32 s40, s42, s45
	v_and_b32_e32 v48, 0xffff0000, v48
	v_mul_f32_e32 v1, 0x3fb8aa3b, v1
	s_add_i32 s40, s40, s44
	v_lshlrev_b32_e32 v61, 16, v49
	v_and_b32_e32 v49, 0xffff0000, v49
	v_lshlrev_b32_e32 v70, 16, v6
	v_and_b32_e32 v71, 0xffff0000, v6
	v_mul_f32_e32 v6, 0x3fb8aa3b, v48
	v_exp_f32_e32 v74, v1
	v_lshl_or_b32 v1, s40, 11, v59
	v_lshlrev_b32_e32 v32, 16, v44
	v_and_b32_e32 v33, 0xffff0000, v44
	v_lshlrev_b32_e32 v34, 16, v45
	v_and_b32_e32 v35, 0xffff0000, v45
	v_lshlrev_b32_e32 v44, 16, v36
	v_and_b32_e32 v36, 0xffff0000, v36
	v_lshlrev_b32_e32 v45, 16, v37
	v_and_b32_e32 v37, 0xffff0000, v37
	v_lshlrev_b32_e32 v38, 16, v30
	v_and_b32_e32 v39, 0xffff0000, v30
	v_lshlrev_b32_e32 v40, 16, v31
	v_and_b32_e32 v41, 0xffff0000, v31
	v_lshlrev_b32_e32 v30, 16, v28
	v_lshlrev_b32_e32 v31, 16, v29
	v_mul_f32_e32 v48, 0x3fb8aa3b, v49
	v_exp_f32_e32 v75, v6
	v_add_u32_e32 v6, s37, v1
	v_lshlrev_b32_e32 v72, 16, v7
	v_and_b32_e32 v73, 0xffff0000, v7
	v_mul_f32_e32 v7, 0x3fb8aa3b, v61
	v_mul_f32_e32 v61, 0x3fb8aa3b, v44
	v_mul_f32_e32 v79, 0x3fb8aa3b, v36
	v_mul_f32_e32 v80, 0x3fb8aa3b, v45
	v_mul_f32_e32 v81, 0x3fb8aa3b, v37
	v_mul_f32_e32 v82, 0x3fb8aa3b, v30
	v_mul_f32_e32 v84, 0x3fb8aa3b, v31
	v_exp_f32_e32 v77, v48
	global_load_dwordx2 v[48:49], v1, s[16:17]
	global_load_dwordx2 v[44:45], v1, s[18:19]
	global_load_dwordx2 v[36:37], v6, s[16:17]
	global_load_dwordx2 v[30:31], v6, s[18:19]
	v_add_u32_e32 v1, s37, v6
	v_and_b32_e32 v28, 0xffff0000, v28
	v_and_b32_e32 v29, 0xffff0000, v29
	v_lshlrev_b32_e32 v42, 16, v26
	v_and_b32_e32 v43, 0xffff0000, v26
	v_lshlrev_b32_e32 v46, 16, v27
	v_and_b32_e32 v47, 0xffff0000, v27
	v_lshlrev_b32_e32 v26, 16, v24
	v_and_b32_e32 v24, 0xffff0000, v24
	v_lshlrev_b32_e32 v27, 16, v25
	v_and_b32_e32 v25, 0xffff0000, v25
	v_lshlrev_b32_e32 v50, 16, v22
	v_and_b32_e32 v51, 0xffff0000, v22
	v_lshlrev_b32_e32 v52, 16, v23
	v_and_b32_e32 v53, 0xffff0000, v23
	v_lshlrev_b32_e32 v22, 16, v20
	v_lshlrev_b32_e32 v23, 16, v21
	v_add_u32_e32 v6, s37, v1
	v_mul_f32_e32 v83, 0x3fb8aa3b, v28
	v_mul_f32_e32 v85, 0x3fb8aa3b, v29
	v_mul_f32_e32 v86, 0x3fb8aa3b, v26
	v_mul_f32_e32 v87, 0x3fb8aa3b, v24
	v_mul_f32_e32 v88, 0x3fb8aa3b, v27
	v_mul_f32_e32 v89, 0x3fb8aa3b, v25
	v_mul_f32_e32 v90, 0x3fb8aa3b, v22
	v_mul_f32_e32 v92, 0x3fb8aa3b, v23
	global_load_dwordx2 v[28:29], v1, s[16:17]
	global_load_dwordx2 v[26:27], v1, s[18:19]
	global_load_dwordx2 v[24:25], v6, s[16:17]
	global_load_dwordx2 v[22:23], v6, s[18:19]
	v_add_u32_e32 v1, s37, v6
	v_and_b32_e32 v20, 0xffff0000, v20
	v_and_b32_e32 v21, 0xffff0000, v21
	v_lshlrev_b32_e32 v54, 16, v18
	v_and_b32_e32 v55, 0xffff0000, v18
	v_lshlrev_b32_e32 v56, 16, v19
	v_and_b32_e32 v57, 0xffff0000, v19
	v_lshlrev_b32_e32 v18, 16, v16
	v_and_b32_e32 v16, 0xffff0000, v16
	v_lshlrev_b32_e32 v19, 16, v17
	v_and_b32_e32 v17, 0xffff0000, v17
	v_lshlrev_b32_e32 v62, 16, v14
	v_and_b32_e32 v63, 0xffff0000, v14
	v_lshlrev_b32_e32 v64, 16, v15
	v_and_b32_e32 v65, 0xffff0000, v15
	v_lshlrev_b32_e32 v14, 16, v12
	v_lshlrev_b32_e32 v15, 16, v13
	v_add_u32_e32 v6, s37, v1
	v_mul_f32_e32 v91, 0x3fb8aa3b, v20
	v_mul_f32_e32 v93, 0x3fb8aa3b, v21
	v_mul_f32_e32 v94, 0x3fb8aa3b, v18
	v_mul_f32_e32 v95, 0x3fb8aa3b, v16
	v_mul_f32_e32 v96, 0x3fb8aa3b, v19
	v_mul_f32_e32 v97, 0x3fb8aa3b, v17
	v_mul_f32_e32 v98, 0x3fb8aa3b, v14
	v_mul_f32_e32 v100, 0x3fb8aa3b, v15
	global_load_dwordx2 v[20:21], v1, s[16:17]
	global_load_dwordx2 v[18:19], v1, s[18:19]
	global_load_dwordx2 v[16:17], v6, s[16:17]
	global_load_dwordx2 v[14:15], v6, s[18:19]
	v_add_u32_e32 v1, s37, v6
	v_and_b32_e32 v12, 0xffff0000, v12
	v_and_b32_e32 v13, 0xffff0000, v13
	v_lshlrev_b32_e32 v66, 16, v10
	v_and_b32_e32 v67, 0xffff0000, v10
	v_lshlrev_b32_e32 v68, 16, v11
	v_and_b32_e32 v69, 0xffff0000, v11
	v_lshlrev_b32_e32 v10, 16, v8
	v_and_b32_e32 v8, 0xffff0000, v8
	v_lshlrev_b32_e32 v11, 16, v9
	v_and_b32_e32 v9, 0xffff0000, v9
	v_add_u32_e32 v6, s37, v1
	v_mul_f32_e32 v99, 0x3fb8aa3b, v12
	v_mul_f32_e32 v101, 0x3fb8aa3b, v13
	v_mul_f32_e32 v102, 0x3fb8aa3b, v10
	v_mul_f32_e32 v103, 0x3fb8aa3b, v8
	v_mul_f32_e32 v104, 0x3fb8aa3b, v11
	v_mul_f32_e32 v105, 0x3fb8aa3b, v9
	v_exp_f32_e32 v76, v7
	global_load_dwordx2 v[12:13], v1, s[16:17]
	global_load_dwordx2 v[10:11], v1, s[18:19]
	global_load_dwordx2 v[8:9], v6, s[16:17]
	s_nop 0
	global_load_dwordx2 v[6:7], v6, s[18:19]
	v_exp_f32_e32 v78, v61
	v_exp_f32_e32 v79, v79
	v_exp_f32_e32 v80, v80
	v_exp_f32_e32 v81, v81
	v_exp_f32_e32 v82, v82
	v_exp_f32_e32 v83, v83
	v_exp_f32_e32 v84, v84
	v_exp_f32_e32 v85, v85
	v_exp_f32_e32 v86, v86
	v_exp_f32_e32 v87, v87
	v_exp_f32_e32 v88, v88
	v_exp_f32_e32 v89, v89
	v_exp_f32_e32 v90, v90
	v_exp_f32_e32 v91, v91
	v_pk_fma_f32 v[2:3], v[2:3], v[74:75], v[32:33]
	v_exp_f32_e32 v92, v92
	v_exp_f32_e32 v93, v93
	v_pk_fma_f32 v[4:5], v[4:5], v[76:77], v[34:35]
	v_cvt_pk_bf16_f32 v32, v2, v3
	v_pk_fma_f32 v[2:3], v[78:79], v[2:3], v[38:39]
	v_exp_f32_e32 v94, v94
	v_exp_f32_e32 v95, v95
	v_exp_f32_e32 v96, v96
	v_exp_f32_e32 v97, v97
	v_cvt_pk_bf16_f32 v33, v4, v5
	v_pk_fma_f32 v[4:5], v[80:81], v[4:5], v[40:41]
	v_cvt_pk_bf16_f32 v34, v2, v3
	v_pk_fma_f32 v[2:3], v[82:83], v[2:3], v[42:43]
	v_lshl_or_b32 v1, s43, 11, v59
	v_exp_f32_e32 v98, v98
	v_exp_f32_e32 v99, v99
	v_exp_f32_e32 v100, v100
	v_exp_f32_e32 v101, v101
	v_cvt_pk_bf16_f32 v35, v4, v5
	v_pk_fma_f32 v[4:5], v[84:85], v[4:5], v[46:47]
	v_cvt_pk_bf16_f32 v38, v2, v3
	v_pk_fma_f32 v[2:3], v[86:87], v[2:3], v[50:51]
	v_add_u32_e32 v61, s37, v1
	v_exp_f32_e32 v102, v102
	v_exp_f32_e32 v103, v103
	v_exp_f32_e32 v104, v104
	v_exp_f32_e32 v105, v105
	v_cvt_pk_bf16_f32 v39, v4, v5
	v_pk_fma_f32 v[4:5], v[88:89], v[4:5], v[52:53]
	v_cvt_pk_bf16_f32 v40, v2, v3
	v_pk_fma_f32 v[2:3], v[90:91], v[2:3], v[54:55]
	v_add_u32_e32 v54, s37, v61
	v_cvt_pk_bf16_f32 v41, v4, v5
	v_pk_fma_f32 v[4:5], v[92:93], v[4:5], v[56:57]
	v_add_u32_e32 v55, s37, v54
	v_cvt_pk_bf16_f32 v42, v2, v3
	v_cvt_pk_bf16_f32 v43, v4, v5
	v_pk_fma_f32 v[4:5], v[96:97], v[4:5], v[64:65]
	v_pk_fma_f32 v[2:3], v[94:95], v[2:3], v[62:63]
	v_add_u32_e32 v56, s37, v55
	v_cvt_pk_bf16_f32 v46, v2, v3
	v_cvt_pk_bf16_f32 v47, v4, v5
	v_pk_fma_f32 v[4:5], v[100:101], v[4:5], v[68:69]
	v_pk_fma_f32 v[2:3], v[98:99], v[2:3], v[66:67]
	s_add_i32 s39, s39, 8
	v_add_u32_e32 v57, s37, v56
	v_cvt_pk_bf16_f32 v50, v2, v3
	v_cvt_pk_bf16_f32 v51, v4, v5
	v_pk_fma_f32 v[4:5], v[104:105], v[4:5], v[72:73]
	v_pk_fma_f32 v[2:3], v[102:103], v[2:3], v[70:71]
	v_add_u32_e32 v62, s37, v57
	s_cmpk_lg_i32 s39, 0x80
	v_cvt_pk_bf16_f32 v52, v2, v3
	v_cvt_pk_bf16_f32 v53, v4, v5
	v_add_u32_e32 v63, s37, v62
	global_store_dwordx2 v1, v[32:33], s[14:15]
	global_store_dwordx2 v61, v[34:35], s[14:15]
	global_store_dwordx2 v54, v[38:39], s[14:15]
	global_store_dwordx2 v55, v[40:41], s[14:15]
	global_store_dwordx2 v56, v[42:43], s[14:15]
	global_store_dwordx2 v57, v[46:47], s[14:15]
	global_store_dwordx2 v62, v[50:51], s[14:15]
	global_store_dwordx2 v63, v[52:53], s[14:15]
	s_cbranch_scc1 .LBB0_652
	s_waitcnt vmcnt(23)
	v_lshlrev_b32_e32 v1, 16, v48
	v_and_b32_e32 v35, 0xffff0000, v48
	v_lshlrev_b32_e32 v38, 16, v49
	v_mul_f32_e32 v1, 0x3fb8aa3b, v1
	v_and_b32_e32 v39, 0xffff0000, v49
	v_exp_f32_e32 v34, v1
	v_mul_f32_e32 v1, 0x3fb8aa3b, v35
	v_mul_f32_e32 v35, 0x3fb8aa3b, v38
	v_exp_f32_e32 v38, v35
	v_mul_f32_e32 v35, 0x3fb8aa3b, v39
	v_exp_f32_e32 v39, v35
	v_exp_f32_e32 v35, v1
	s_waitcnt vmcnt(22)
	v_lshlrev_b32_e32 v40, 16, v45
	v_and_b32_e32 v41, 0xffff0000, v45
	s_waitcnt vmcnt(21)
	v_lshlrev_b32_e32 v1, 16, v36
	v_lshlrev_b32_e32 v32, 16, v44
	v_and_b32_e32 v33, 0xffff0000, v44
	v_pk_fma_f32 v[4:5], v[38:39], v[4:5], v[40:41]
	v_and_b32_e32 v38, 0xffff0000, v36
	v_lshlrev_b32_e32 v39, 16, v37
	v_mul_f32_e32 v1, 0x3fb8aa3b, v1
	v_pk_fma_f32 v[2:3], v[34:35], v[2:3], v[32:33]
	v_and_b32_e32 v37, 0xffff0000, v37
	s_waitcnt vmcnt(20)
	v_lshlrev_b32_e32 v34, 16, v30
	v_and_b32_e32 v35, 0xffff0000, v30
	v_exp_f32_e32 v36, v1
	v_mul_f32_e32 v1, 0x3fb8aa3b, v38
	v_mul_f32_e32 v30, 0x3fb8aa3b, v39
	v_exp_f32_e32 v38, v30
	v_mul_f32_e32 v30, 0x3fb8aa3b, v37
	v_exp_f32_e32 v37, v1
	s_waitcnt vmcnt(19)
	v_lshlrev_b32_e32 v1, 16, v28
	v_cvt_pk_bf16_f32 v32, v2, v3
	v_mul_f32_e32 v1, 0x3fb8aa3b, v1
	v_pk_fma_f32 v[2:3], v[36:37], v[2:3], v[34:35]
	v_and_b32_e32 v35, 0xffff0000, v28
	v_exp_f32_e32 v34, v1
	v_mul_f32_e32 v1, 0x3fb8aa3b, v35
	v_exp_f32_e32 v39, v30
	v_exp_f32_e32 v35, v1
	v_lshlrev_b32_e32 v30, 16, v31
	v_and_b32_e32 v31, 0xffff0000, v31
	v_lshlrev_b32_e32 v36, 16, v29
	v_and_b32_e32 v37, 0xffff0000, v29
	s_waitcnt vmcnt(18)
	v_lshlrev_b32_e32 v28, 16, v26
	v_and_b32_e32 v29, 0xffff0000, v26
	s_waitcnt vmcnt(17)
	v_lshlrev_b32_e32 v1, 16, v24
	v_cvt_pk_bf16_f32 v33, v4, v5
	v_pk_fma_f32 v[4:5], v[38:39], v[4:5], v[30:31]
	v_cvt_pk_bf16_f32 v30, v2, v3
	v_mul_f32_e32 v26, 0x3fb8aa3b, v36
	v_pk_fma_f32 v[2:3], v[34:35], v[2:3], v[28:29]
	v_and_b32_e32 v29, 0xffff0000, v24
	v_mul_f32_e32 v1, 0x3fb8aa3b, v1
	v_exp_f32_e32 v36, v26
	v_mul_f32_e32 v26, 0x3fb8aa3b, v37
	v_exp_f32_e32 v28, v1
	v_mul_f32_e32 v1, 0x3fb8aa3b, v29
	v_exp_f32_e32 v37, v26
	v_exp_f32_e32 v29, v1
	v_lshlrev_b32_e32 v26, 16, v27
	v_and_b32_e32 v27, 0xffff0000, v27
	v_lshlrev_b32_e32 v34, 16, v25
	v_and_b32_e32 v35, 0xffff0000, v25
	s_waitcnt vmcnt(16)
	v_lshlrev_b32_e32 v24, 16, v22
	v_and_b32_e32 v25, 0xffff0000, v22
	s_waitcnt vmcnt(15)
	v_lshlrev_b32_e32 v1, 16, v20
	v_cvt_pk_bf16_f32 v31, v4, v5
	v_pk_fma_f32 v[4:5], v[36:37], v[4:5], v[26:27]
	v_cvt_pk_bf16_f32 v26, v2, v3
	v_mul_f32_e32 v22, 0x3fb8aa3b, v34
	v_pk_fma_f32 v[2:3], v[28:29], v[2:3], v[24:25]
	v_and_b32_e32 v25, 0xffff0000, v20
	v_mul_f32_e32 v1, 0x3fb8aa3b, v1
	v_exp_f32_e32 v34, v22
	v_mul_f32_e32 v22, 0x3fb8aa3b, v35
	v_exp_f32_e32 v24, v1
	v_mul_f32_e32 v1, 0x3fb8aa3b, v25
	v_exp_f32_e32 v35, v22
	v_exp_f32_e32 v25, v1
	v_lshlrev_b32_e32 v22, 16, v23
	v_and_b32_e32 v23, 0xffff0000, v23
	v_lshlrev_b32_e32 v28, 16, v21
	v_and_b32_e32 v29, 0xffff0000, v21
	s_waitcnt vmcnt(14)
	v_lshlrev_b32_e32 v20, 16, v18
	v_and_b32_e32 v21, 0xffff0000, v18
	s_waitcnt vmcnt(13)
	v_lshlrev_b32_e32 v1, 16, v16
	v_cvt_pk_bf16_f32 v27, v4, v5
	v_pk_fma_f32 v[4:5], v[34:35], v[4:5], v[22:23]
	v_cvt_pk_bf16_f32 v22, v2, v3
	v_mul_f32_e32 v18, 0x3fb8aa3b, v28
	v_pk_fma_f32 v[2:3], v[24:25], v[2:3], v[20:21]
	v_and_b32_e32 v21, 0xffff0000, v16
	v_mul_f32_e32 v1, 0x3fb8aa3b, v1
	v_exp_f32_e32 v28, v18
	v_mul_f32_e32 v18, 0x3fb8aa3b, v29
	v_exp_f32_e32 v20, v1
	v_mul_f32_e32 v1, 0x3fb8aa3b, v21
	v_exp_f32_e32 v29, v18
	v_exp_f32_e32 v21, v1
	v_lshlrev_b32_e32 v18, 16, v19
	v_and_b32_e32 v19, 0xffff0000, v19
	v_lshlrev_b32_e32 v24, 16, v17
	v_and_b32_e32 v25, 0xffff0000, v17
	s_waitcnt vmcnt(12)
	v_lshlrev_b32_e32 v16, 16, v14
	v_and_b32_e32 v17, 0xffff0000, v14
	s_waitcnt vmcnt(11)
	v_lshlrev_b32_e32 v1, 16, v12
	v_cvt_pk_bf16_f32 v23, v4, v5
	v_pk_fma_f32 v[4:5], v[28:29], v[4:5], v[18:19]
	v_cvt_pk_bf16_f32 v18, v2, v3
	v_mul_f32_e32 v14, 0x3fb8aa3b, v24
	v_pk_fma_f32 v[2:3], v[20:21], v[2:3], v[16:17]
	v_and_b32_e32 v17, 0xffff0000, v12
	v_mul_f32_e32 v1, 0x3fb8aa3b, v1
	v_exp_f32_e32 v24, v14
	v_mul_f32_e32 v14, 0x3fb8aa3b, v25
	v_exp_f32_e32 v16, v1
	v_mul_f32_e32 v1, 0x3fb8aa3b, v17
	v_exp_f32_e32 v25, v14
	v_exp_f32_e32 v17, v1
	s_cmp_lt_i32 s33, 1
	s_cselect_b32 s16, 0x80, s29
	s_cselect_b32 s17, s30, 0x107f
	s_cselect_b32 s18, s36, s35
	s_add_i32 s16, s16, s34
	s_sub_i32 s17, s17, s34
	v_lshlrev_b32_e32 v14, 16, v15
	v_and_b32_e32 v15, 0xffff0000, v15
	v_lshlrev_b32_e32 v20, 16, v13
	v_and_b32_e32 v21, 0xffff0000, v13
	s_waitcnt vmcnt(10)
	v_lshlrev_b32_e32 v12, 16, v10
	v_and_b32_e32 v13, 0xffff0000, v10
	s_waitcnt vmcnt(9)
	v_lshlrev_b32_e32 v1, 16, v8
	s_and_b64 s[12:13], s[12:13], exec
	v_cvt_pk_bf16_f32 v19, v4, v5
	v_pk_fma_f32 v[4:5], v[24:25], v[4:5], v[14:15]
	v_cvt_pk_bf16_f32 v14, v2, v3
	v_pk_fma_f32 v[2:3], v[16:17], v[2:3], v[12:13]
	v_and_b32_e32 v13, 0xffff0000, v8
	v_mul_f32_e32 v1, 0x3fb8aa3b, v1
	s_cselect_b32 s12, s16, s17
	v_mul_f32_e32 v10, 0x3fb8aa3b, v20
	v_lshlrev_b32_e32 v16, 16, v9
	v_exp_f32_e32 v12, v1
	v_mul_f32_e32 v1, 0x3fb8aa3b, v13
	s_add_i32 s18, s18, s12
	v_exp_f32_e32 v20, v10
	v_mul_f32_e32 v10, 0x3fb8aa3b, v21
	v_and_b32_e32 v17, 0xffff0000, v9
	s_waitcnt vmcnt(8)
	v_lshlrev_b32_e32 v8, 16, v6
	v_and_b32_e32 v9, 0xffff0000, v6
	v_mul_f32_e32 v6, 0x3fb8aa3b, v16
	v_exp_f32_e32 v13, v1
	v_lshl_or_b32 v1, s18, 11, v59
	v_exp_f32_e32 v21, v10
	v_exp_f32_e32 v16, v6
	v_mul_f32_e32 v6, 0x3fb8aa3b, v17
	global_store_dwordx2 v1, v[32:33], s[14:15]
	v_add_u32_e32 v1, s37, v1
	v_exp_f32_e32 v17, v6
	global_store_dwordx2 v1, v[30:31], s[14:15]
	v_add_u32_e32 v1, s37, v1
	global_store_dwordx2 v1, v[26:27], s[14:15]
	v_add_u32_e32 v1, s37, v1
	v_lshlrev_b32_e32 v10, 16, v11
	v_and_b32_e32 v11, 0xffff0000, v11
	global_store_dwordx2 v1, v[22:23], s[14:15]
	v_add_u32_e32 v1, s37, v1
	v_cvt_pk_bf16_f32 v15, v4, v5
	v_pk_fma_f32 v[4:5], v[20:21], v[4:5], v[10:11]
	v_lshlrev_b32_e32 v6, 16, v7
	v_and_b32_e32 v7, 0xffff0000, v7
	global_store_dwordx2 v1, v[18:19], s[14:15]
	v_add_u32_e32 v1, s37, v1
	v_add_u32_e32 v58, s20, v58
	v_cvt_pk_bf16_f32 v10, v2, v3
	v_cvt_pk_bf16_f32 v11, v4, v5
	v_pk_fma_f32 v[4:5], v[16:17], v[4:5], v[6:7]
	v_pk_fma_f32 v[2:3], v[12:13], v[2:3], v[8:9]
	global_store_dwordx2 v1, v[14:15], s[14:15]
	v_add_u32_e32 v1, s37, v1
	v_cmp_lt_i32_e32 vcc, s31, v58
	v_cvt_pk_bf16_f32 v2, v2, v3
	v_cvt_pk_bf16_f32 v3, v4, v5
	global_store_dwordx2 v1, v[10:11], s[14:15]
	v_add_u32_e32 v1, s37, v1
	s_or_b64 s[10:11], vcc, s[10:11]
	global_store_dwordx2 v1, v[2:3], s[14:15]
	s_andn2_b64 exec, exec, s[10:11]
	s_cbranch_execnz .LBB0_643

.LBB0_1356:
	s_cmp_lt_i32 s88, 14
	s_cselect_b64 s[2:3], -1, 0
	s_and_b64 s[4:5], s[2:3], s[4:5]
	s_andn2_b64 vcc, exec, s[4:5]
	s_cbranch_vccnz .LBB0_1694
	v_mbcnt_lo_u32_b32 v0, -1, 0
	v_mbcnt_hi_u32_b32 v0, -1, v0
	s_mov_b64 s[8:9], s[86:87]
	s_waitcnt vmcnt(0)
	v_lshl_or_b32 v10, s96, 6, v0
	v_readlane_b32 s4, v254, 0
	s_load_dword s5, s[0:1], 0x108
	s_add_u32 s6, s8, 0x1000
	s_addc_u32 s7, s9, 0
	v_cmp_eq_u32_e32 vcc, 0, v10
	s_and_saveexec_b64 s[10:11], vcc
	s_cbranch_execz .LBB0_1678
	v_mov_b32_e32 v4, 0
	global_load_dwordx4 v[100:103], v4, s[6:7] sc1
	global_load_dwordx4 v[104:107], v4, s[6:7] offset:16 sc1
	global_load_dwordx4 v[108:111], v4, s[6:7] offset:32 sc1
	global_load_dwordx4 v[112:115], v4, s[6:7] offset:48 sc1
	global_load_dwordx4 v[116:119], v4, s[6:7] offset:64 sc1
	global_load_dwordx4 v[120:123], v4, s[6:7] offset:80 sc1
	global_load_dwordx4 v[124:127], v4, s[6:7] offset:96 sc1
	global_load_dwordx4 v[128:131], v4, s[6:7] offset:112 sc1
	s_waitcnt vmcnt(0)
	v_mov_b32_e32 v0, v100
	v_mov_b32_e32 v1, 0
	s_cmp_eq_u32 s4, 0
	s_movk_i32 s16, 0xff
	ds_write_b32 v4, v1
	s_cselect_b64 s[12:13], -1, 0
	v_add_u32_e32 v1, 0xff, v0
	v_cmp_lt_u32_e32 vcc, s16, v1
	s_and_b64 s[14:15], s[12:13], vcc
	s_andn2_b64 vcc, exec, s[14:15]
	v_lshrrev_b32_e32 v0, 8, v1
	s_cbranch_vccnz .LBB0_1366
	s_movk_i32 s14, 0x200
	v_cmp_gt_u32_e32 vcc, s14, v1
	s_mov_b64 s[14:15], -1
	s_cbranch_vccnz .LBB0_1363
	s_add_u32 s14, s8, 0x2000
	v_and_b32_e32 v4, 0xfffffe, v0
	v_mov_b32_e32 v2, 0
	s_addc_u32 s15, s9, 0
	v_mov_b32_e32 v3, v2
	v_mov_b32_e32 v5, v4

.LBB0_1366:
	v_mov_b32_e32 v11, 0x1000
	v_mov_b32_e32 v2, v101
	v_and_b32_e32 v9, 0xffffff00, v1
	v_mov_b32_e32 v8, 0
	ds_write_b32 v8, v9 offset:4
	v_add_u32_e32 v12, 0xff, v2
	v_cmp_lt_u32_e32 vcc, s16, v12
	s_and_b64 s[14:15], s[12:13], vcc
	s_andn2_b64 vcc, exec, s[14:15]
	s_cbranch_vccnz .LBB0_1376
	s_movk_i32 s14, 0x1ff
	v_cmp_lt_u32_e32 vcc, s14, v12
	v_lshrrev_b32_e32 v3, 8, v12
	s_cbranch_vccz .LBB0_1371
	v_mov_b32_e32 v1, 0
	v_lshlrev_b32_e32 v4, 2, v0
	v_mov_b32_e32 v5, v1
	v_and_b32_e32 v2, 0xfffffe, v3
	v_lshl_add_u64 v[4:5], s[8:9], 0, v[4:5]
	s_mov_b64 s[14:15], 0x2000
	v_mov_b32_e32 v6, 1
	v_lshl_add_u64 v[4:5], v[4:5], 0, s[14:15]
	v_mov_b32_e32 v7, v6
	v_mov_b32_e32 v13, v2

.LBB0_1376:
	v_mov_b32_e32 v1, v102
	s_movk_i32 s18, 0xff
	v_and_b32_e32 v0, 0xffffff00, v12
	v_add_u32_e32 v0, v0, v9
	ds_write_b32 v8, v0 offset:8
	v_add_u32_e32 v1, 0xff, v1
	v_cmp_lt_u32_e32 vcc, s18, v1
	s_and_b64 s[14:15], s[12:13], vcc
	s_andn2_b64 vcc, exec, s[14:15]
	s_cbranch_vccnz .LBB0_1386
	s_movk_i32 s14, 0x1ff
	v_cmp_lt_u32_e32 vcc, s14, v1
	v_lshrrev_b32_e32 v3, 8, v1
	v_mov_b32_e32 v5, 0
	s_cbranch_vccz .LBB0_1381
	v_lshrrev_b32_e32 v4, 6, v0
	v_and_b32_e32 v2, 0xfffffe, v3
	v_lshl_add_u64 v[4:5], s[8:9], 0, v[4:5]
	s_mov_b64 s[14:15], 0x2000
	v_mov_b32_e32 v6, 2
	v_lshl_add_u64 v[4:5], v[4:5], 0, s[14:15]
	v_mov_b32_e32 v7, v6
	v_mov_b32_e32 v8, v2

.LBB0_1386:
	v_mov_b32_e32 v3, 0x1000
	v_mov_b32_e32 v4, v103
	v_and_b32_e32 v2, 0xffffff00, v1
	v_mov_b32_e32 v1, 0
	v_add_u32_e32 v2, v2, v0
	ds_write_b32 v1, v2 offset:12
	s_waitcnt vmcnt(0)
	v_add_u32_e32 v11, 0xff, v4
	v_cmp_lt_u32_e32 vcc, s18, v11
	s_and_b64 s[14:15], s[12:13], vcc
	s_andn2_b64 vcc, exec, s[14:15]
	s_cbranch_vccnz .LBB0_1396
	s_movk_i32 s14, 0x1ff
	v_cmp_lt_u32_e32 vcc, s14, v11
	v_lshrrev_b32_e32 v5, 8, v11
	s_cbranch_vccz .LBB0_1391
	v_lshrrev_b32_e32 v0, 6, v2
	v_and_b32_e32 v4, 0xfffffe, v5
	v_lshl_add_u64 v[6:7], s[8:9], 0, v[0:1]
	s_mov_b64 s[14:15], 0x2000
	v_mov_b32_e32 v8, 3
	v_lshl_add_u64 v[6:7], v[6:7], 0, s[14:15]
	v_mov_b32_e32 v9, v8
	v_mov_b32_e32 v0, v4

.LBB0_1396:
	v_mov_b32_e32 v3, v104
	s_movk_i32 s18, 0xff
	v_and_b32_e32 v0, 0xffffff00, v11
	v_add_u32_e32 v0, v0, v2
	ds_write_b32 v1, v0 offset:16
	v_add_u32_e32 v8, 0xff, v3
	v_cmp_lt_u32_e32 vcc, s18, v8
	s_and_b64 s[14:15], s[12:13], vcc
	s_andn2_b64 vcc, exec, s[14:15]
	s_cbranch_vccnz .LBB0_1406
	s_movk_i32 s14, 0x1ff
	v_cmp_lt_u32_e32 vcc, s14, v8
	v_lshrrev_b32_e32 v1, 8, v8
	v_mov_b32_e32 v5, 0
	s_cbranch_vccz .LBB0_1401
	v_lshrrev_b32_e32 v4, 6, v0
	v_and_b32_e32 v2, 0xfffffe, v1
	v_lshl_add_u64 v[4:5], s[8:9], 0, v[4:5]
	s_mov_b64 s[14:15], 0x2000
	v_mov_b32_e32 v6, 4
	v_lshl_add_u64 v[4:5], v[4:5], 0, s[14:15]
	v_mov_b32_e32 v7, v6
	v_mov_b32_e32 v3, v2

.LBB0_1406:
	v_mov_b32_e32 v3, 0x1000
	v_mov_b32_e32 v4, v105
	v_and_b32_e32 v2, 0xffffff00, v8
	v_mov_b32_e32 v1, 0
	v_add_u32_e32 v2, v2, v0
	ds_write_b32 v1, v2 offset:20
	v_add_u32_e32 v11, 0xff, v4
	v_cmp_lt_u32_e32 vcc, s18, v11
	s_and_b64 s[14:15], s[12:13], vcc
	s_andn2_b64 vcc, exec, s[14:15]
	s_cbranch_vccnz .LBB0_1416
	s_movk_i32 s14, 0x1ff
	v_cmp_lt_u32_e32 vcc, s14, v11
	v_lshrrev_b32_e32 v5, 8, v11
	s_cbranch_vccz .LBB0_1411
	v_lshrrev_b32_e32 v0, 6, v2
	v_and_b32_e32 v4, 0xfffffe, v5
	v_lshl_add_u64 v[6:7], s[8:9], 0, v[0:1]
	s_mov_b64 s[14:15], 0x2000
	v_mov_b32_e32 v8, 5
	v_lshl_add_u64 v[6:7], v[6:7], 0, s[14:15]
	v_mov_b32_e32 v9, v8
	v_mov_b32_e32 v0, v4

.LBB0_1416:
	v_mov_b32_e32 v3, v106
	s_movk_i32 s18, 0xff
	v_and_b32_e32 v0, 0xffffff00, v11
	v_add_u32_e32 v0, v0, v2
	ds_write_b32 v1, v0 offset:24
	v_add_u32_e32 v8, 0xff, v3
	v_cmp_lt_u32_e32 vcc, s18, v8
	s_and_b64 s[14:15], s[12:13], vcc
	s_andn2_b64 vcc, exec, s[14:15]
	s_cbranch_vccnz .LBB0_1426
	s_movk_i32 s14, 0x1ff
	v_cmp_lt_u32_e32 vcc, s14, v8
	v_lshrrev_b32_e32 v1, 8, v8
	v_mov_b32_e32 v5, 0
	s_cbranch_vccz .LBB0_1421
	v_lshrrev_b32_e32 v4, 6, v0
	v_and_b32_e32 v2, 0xfffffe, v1
	v_lshl_add_u64 v[4:5], s[8:9], 0, v[4:5]
	s_mov_b64 s[14:15], 0x2000
	v_mov_b32_e32 v6, 6
	v_lshl_add_u64 v[4:5], v[4:5], 0, s[14:15]
	v_mov_b32_e32 v7, v6
	v_mov_b32_e32 v3, v2

.LBB0_1426:
	v_mov_b32_e32 v3, 0x1000
	v_mov_b32_e32 v4, v107
	v_and_b32_e32 v2, 0xffffff00, v8
	v_mov_b32_e32 v1, 0
	v_add_u32_e32 v2, v2, v0
	ds_write_b32 v1, v2 offset:28
	s_waitcnt vmcnt(0)
	v_add_u32_e32 v11, 0xff, v4
	v_cmp_lt_u32_e32 vcc, s18, v11
	s_and_b64 s[14:15], s[12:13], vcc
	s_andn2_b64 vcc, exec, s[14:15]
	s_cbranch_vccnz .LBB0_1436
	s_movk_i32 s14, 0x1ff
	v_cmp_lt_u32_e32 vcc, s14, v11
	v_lshrrev_b32_e32 v5, 8, v11
	s_cbranch_vccz .LBB0_1431
	v_lshrrev_b32_e32 v0, 6, v2
	v_and_b32_e32 v4, 0xfffffe, v5
	v_lshl_add_u64 v[6:7], s[8:9], 0, v[0:1]
	s_mov_b64 s[14:15], 0x2000
	v_mov_b32_e32 v8, 7
	v_lshl_add_u64 v[6:7], v[6:7], 0, s[14:15]
	v_mov_b32_e32 v9, v8
	v_mov_b32_e32 v0, v4

.LBB0_1436:
	v_mov_b32_e32 v3, v108
	s_movk_i32 s18, 0xff
	v_and_b32_e32 v0, 0xffffff00, v11
	v_add_u32_e32 v0, v0, v2
	ds_write_b32 v1, v0 offset:32
	v_add_u32_e32 v8, 0xff, v3
	v_cmp_lt_u32_e32 vcc, s18, v8
	s_and_b64 s[14:15], s[12:13], vcc
	s_andn2_b64 vcc, exec, s[14:15]
	s_cbranch_vccnz .LBB0_1446
	s_movk_i32 s14, 0x1ff
	v_cmp_lt_u32_e32 vcc, s14, v8
	v_lshrrev_b32_e32 v1, 8, v8
	v_mov_b32_e32 v5, 0
	s_cbranch_vccz .LBB0_1441
	v_lshrrev_b32_e32 v4, 6, v0
	v_and_b32_e32 v2, 0xfffffe, v1
	v_lshl_add_u64 v[4:5], s[8:9], 0, v[4:5]
	s_mov_b64 s[14:15], 0x2000
	v_mov_b32_e32 v6, 8
	v_lshl_add_u64 v[4:5], v[4:5], 0, s[14:15]
	v_mov_b32_e32 v7, v6
	v_mov_b32_e32 v3, v2

.LBB0_1446:
	v_mov_b32_e32 v3, 0x1000
	v_mov_b32_e32 v4, v109
	v_and_b32_e32 v2, 0xffffff00, v8
	v_mov_b32_e32 v1, 0
	v_add_u32_e32 v2, v2, v0
	ds_write_b32 v1, v2 offset:36
	v_add_u32_e32 v11, 0xff, v4
	v_cmp_lt_u32_e32 vcc, s18, v11
	s_and_b64 s[14:15], s[12:13], vcc
	s_andn2_b64 vcc, exec, s[14:15]
	s_cbranch_vccnz .LBB0_1456
	s_movk_i32 s14, 0x1ff
	v_cmp_lt_u32_e32 vcc, s14, v11
	v_lshrrev_b32_e32 v5, 8, v11
	s_cbranch_vccz .LBB0_1451
	v_lshrrev_b32_e32 v0, 6, v2
	v_and_b32_e32 v4, 0xfffffe, v5
	v_lshl_add_u64 v[6:7], s[8:9], 0, v[0:1]
	s_mov_b64 s[14:15], 0x2000
	v_mov_b32_e32 v8, 9
	v_lshl_add_u64 v[6:7], v[6:7], 0, s[14:15]
	v_mov_b32_e32 v9, v8
	v_mov_b32_e32 v0, v4

.LBB0_1456:
	v_mov_b32_e32 v3, v110
	s_movk_i32 s18, 0xff
	v_and_b32_e32 v0, 0xffffff00, v11
	v_add_u32_e32 v0, v0, v2
	ds_write_b32 v1, v0 offset:40
	v_add_u32_e32 v8, 0xff, v3
	v_cmp_lt_u32_e32 vcc, s18, v8
	s_and_b64 s[14:15], s[12:13], vcc
	s_andn2_b64 vcc, exec, s[14:15]
	s_cbranch_vccnz .LBB0_1466
	s_movk_i32 s14, 0x1ff
	v_cmp_lt_u32_e32 vcc, s14, v8
	v_lshrrev_b32_e32 v1, 8, v8
	v_mov_b32_e32 v5, 0
	s_cbranch_vccz .LBB0_1461
	v_lshrrev_b32_e32 v4, 6, v0
	v_and_b32_e32 v2, 0xfffffe, v1
	v_lshl_add_u64 v[4:5], s[8:9], 0, v[4:5]
	s_mov_b64 s[14:15], 0x2000
	v_mov_b32_e32 v6, 10
	v_lshl_add_u64 v[4:5], v[4:5], 0, s[14:15]
	v_mov_b32_e32 v7, v6
	v_mov_b32_e32 v3, v2

.LBB0_1466:
	v_mov_b32_e32 v3, 0x1000
	v_mov_b32_e32 v4, v111
	v_and_b32_e32 v2, 0xffffff00, v8
	v_mov_b32_e32 v1, 0
	v_add_u32_e32 v2, v2, v0
	ds_write_b32 v1, v2 offset:44
	s_waitcnt vmcnt(0)
	v_add_u32_e32 v11, 0xff, v4
	v_cmp_lt_u32_e32 vcc, s18, v11
	s_and_b64 s[14:15], s[12:13], vcc
	s_andn2_b64 vcc, exec, s[14:15]
	s_cbranch_vccnz .LBB0_1476
	s_movk_i32 s14, 0x1ff
	v_cmp_lt_u32_e32 vcc, s14, v11
	v_lshrrev_b32_e32 v5, 8, v11
	s_cbranch_vccz .LBB0_1471
	v_lshrrev_b32_e32 v0, 6, v2
	v_and_b32_e32 v4, 0xfffffe, v5
	v_lshl_add_u64 v[6:7], s[8:9], 0, v[0:1]
	s_mov_b64 s[14:15], 0x2000
	v_mov_b32_e32 v8, 11
	v_lshl_add_u64 v[6:7], v[6:7], 0, s[14:15]
	v_mov_b32_e32 v9, v8
	v_mov_b32_e32 v0, v4

.LBB0_1476:
	v_mov_b32_e32 v3, v112
	s_movk_i32 s18, 0xff
	v_and_b32_e32 v0, 0xffffff00, v11
	v_add_u32_e32 v0, v0, v2
	ds_write_b32 v1, v0 offset:48
	v_add_u32_e32 v8, 0xff, v3
	v_cmp_lt_u32_e32 vcc, s18, v8
	s_and_b64 s[14:15], s[12:13], vcc
	s_andn2_b64 vcc, exec, s[14:15]
	s_cbranch_vccnz .LBB0_1486
	s_movk_i32 s14, 0x1ff
	v_cmp_lt_u32_e32 vcc, s14, v8
	v_lshrrev_b32_e32 v1, 8, v8
	v_mov_b32_e32 v5, 0
	s_cbranch_vccz .LBB0_1481
	v_lshrrev_b32_e32 v4, 6, v0
	v_and_b32_e32 v2, 0xfffffe, v1
	v_lshl_add_u64 v[4:5], s[8:9], 0, v[4:5]
	s_mov_b64 s[14:15], 0x2000
	v_mov_b32_e32 v6, 12
	v_lshl_add_u64 v[4:5], v[4:5], 0, s[14:15]
	v_mov_b32_e32 v7, v6
	v_mov_b32_e32 v3, v2

.LBB0_1486:
	v_mov_b32_e32 v3, 0x1000
	v_mov_b32_e32 v4, v113
	v_and_b32_e32 v2, 0xffffff00, v8
	v_mov_b32_e32 v1, 0
	v_add_u32_e32 v2, v2, v0
	ds_write_b32 v1, v2 offset:52
	v_add_u32_e32 v11, 0xff, v4
	v_cmp_lt_u32_e32 vcc, s18, v11
	s_and_b64 s[14:15], s[12:13], vcc
	s_andn2_b64 vcc, exec, s[14:15]
	s_cbranch_vccnz .LBB0_1496
	s_movk_i32 s14, 0x1ff
	v_cmp_lt_u32_e32 vcc, s14, v11
	v_lshrrev_b32_e32 v5, 8, v11
	s_cbranch_vccz .LBB0_1491
	v_lshrrev_b32_e32 v0, 6, v2
	v_and_b32_e32 v4, 0xfffffe, v5
	v_lshl_add_u64 v[6:7], s[8:9], 0, v[0:1]
	s_mov_b64 s[14:15], 0x2000
	v_mov_b32_e32 v8, 13
	v_lshl_add_u64 v[6:7], v[6:7], 0, s[14:15]
	v_mov_b32_e32 v9, v8
	v_mov_b32_e32 v0, v4

.LBB0_1496:
	v_mov_b32_e32 v3, v114
	s_movk_i32 s18, 0xff
	v_and_b32_e32 v0, 0xffffff00, v11
	v_add_u32_e32 v0, v0, v2
	ds_write_b32 v1, v0 offset:56
	v_add_u32_e32 v8, 0xff, v3
	v_cmp_lt_u32_e32 vcc, s18, v8
	s_and_b64 s[14:15], s[12:13], vcc
	s_andn2_b64 vcc, exec, s[14:15]
	s_cbranch_vccnz .LBB0_1506
	s_movk_i32 s14, 0x1ff
	v_cmp_lt_u32_e32 vcc, s14, v8
	v_lshrrev_b32_e32 v1, 8, v8
	v_mov_b32_e32 v5, 0
	s_cbranch_vccz .LBB0_1501
	v_lshrrev_b32_e32 v4, 6, v0
	v_and_b32_e32 v2, 0xfffffe, v1
	v_lshl_add_u64 v[4:5], s[8:9], 0, v[4:5]
	s_mov_b64 s[14:15], 0x2000
	v_mov_b32_e32 v6, 14
	v_lshl_add_u64 v[4:5], v[4:5], 0, s[14:15]
	v_mov_b32_e32 v7, v6
	v_mov_b32_e32 v3, v2

.LBB0_1506:
	v_mov_b32_e32 v3, 0x1000
	v_mov_b32_e32 v4, v115
	v_and_b32_e32 v2, 0xffffff00, v8
	v_mov_b32_e32 v1, 0
	v_add_u32_e32 v2, v2, v0
	ds_write_b32 v1, v2 offset:60
	s_waitcnt vmcnt(0)
	v_add_u32_e32 v11, 0xff, v4
	v_cmp_lt_u32_e32 vcc, s18, v11
	s_and_b64 s[14:15], s[12:13], vcc
	s_andn2_b64 vcc, exec, s[14:15]
	s_cbranch_vccnz .LBB0_1516
	s_movk_i32 s14, 0x1ff
	v_cmp_lt_u32_e32 vcc, s14, v11
	v_lshrrev_b32_e32 v5, 8, v11
	s_cbranch_vccz .LBB0_1511
	v_lshrrev_b32_e32 v0, 6, v2
	v_and_b32_e32 v4, 0xfffffe, v5
	v_lshl_add_u64 v[6:7], s[8:9], 0, v[0:1]
	s_mov_b64 s[14:15], 0x2000
	v_mov_b32_e32 v8, 15
	v_lshl_add_u64 v[6:7], v[6:7], 0, s[14:15]
	v_mov_b32_e32 v9, v8
	v_mov_b32_e32 v0, v4

.LBB0_1516:
	v_mov_b32_e32 v3, v116
	s_movk_i32 s18, 0xff
	v_and_b32_e32 v0, 0xffffff00, v11
	v_add_u32_e32 v0, v0, v2
	ds_write_b32 v1, v0 offset:64
	v_add_u32_e32 v8, 0xff, v3
	v_cmp_lt_u32_e32 vcc, s18, v8
	s_and_b64 s[14:15], s[12:13], vcc
	s_andn2_b64 vcc, exec, s[14:15]
	s_cbranch_vccnz .LBB0_1526
	s_movk_i32 s14, 0x1ff
	v_cmp_lt_u32_e32 vcc, s14, v8
	v_lshrrev_b32_e32 v1, 8, v8
	v_mov_b32_e32 v5, 0
	s_cbranch_vccz .LBB0_1521
	v_lshrrev_b32_e32 v4, 6, v0
	v_and_b32_e32 v2, 0xfffffe, v1
	v_lshl_add_u64 v[4:5], s[8:9], 0, v[4:5]
	s_mov_b64 s[14:15], 0x2000
	v_mov_b32_e32 v6, 16
	v_lshl_add_u64 v[4:5], v[4:5], 0, s[14:15]
	v_mov_b32_e32 v7, v6
	v_mov_b32_e32 v3, v2

.LBB0_1526:
	v_mov_b32_e32 v3, 0x1000
	v_mov_b32_e32 v4, v117
	v_and_b32_e32 v2, 0xffffff00, v8
	v_mov_b32_e32 v1, 0
	v_add_u32_e32 v2, v2, v0
	ds_write_b32 v1, v2 offset:68
	v_add_u32_e32 v11, 0xff, v4
	v_cmp_lt_u32_e32 vcc, s18, v11
	s_and_b64 s[14:15], s[12:13], vcc
	s_andn2_b64 vcc, exec, s[14:15]
	s_cbranch_vccnz .LBB0_1536
	s_movk_i32 s14, 0x1ff
	v_cmp_lt_u32_e32 vcc, s14, v11
	v_lshrrev_b32_e32 v5, 8, v11
	s_cbranch_vccz .LBB0_1531
	v_lshrrev_b32_e32 v0, 6, v2
	v_and_b32_e32 v4, 0xfffffe, v5
	v_lshl_add_u64 v[6:7], s[8:9], 0, v[0:1]
	s_mov_b64 s[14:15], 0x2000
	v_mov_b32_e32 v8, 17
	v_lshl_add_u64 v[6:7], v[6:7], 0, s[14:15]
	v_mov_b32_e32 v9, v8
	v_mov_b32_e32 v0, v4

.LBB0_1536:
	v_mov_b32_e32 v3, v118
	s_movk_i32 s18, 0xff
	v_and_b32_e32 v0, 0xffffff00, v11
	v_add_u32_e32 v0, v0, v2
	ds_write_b32 v1, v0 offset:72
	v_add_u32_e32 v8, 0xff, v3
	v_cmp_lt_u32_e32 vcc, s18, v8
	s_and_b64 s[14:15], s[12:13], vcc
	s_andn2_b64 vcc, exec, s[14:15]
	s_cbranch_vccnz .LBB0_1546
	s_movk_i32 s14, 0x1ff
	v_cmp_lt_u32_e32 vcc, s14, v8
	v_lshrrev_b32_e32 v1, 8, v8
	v_mov_b32_e32 v5, 0
	s_cbranch_vccz .LBB0_1541
	v_lshrrev_b32_e32 v4, 6, v0
	v_and_b32_e32 v2, 0xfffffe, v1
	v_lshl_add_u64 v[4:5], s[8:9], 0, v[4:5]
	s_mov_b64 s[14:15], 0x2000
	v_mov_b32_e32 v6, 18
	v_lshl_add_u64 v[4:5], v[4:5], 0, s[14:15]
	v_mov_b32_e32 v7, v6
	v_mov_b32_e32 v3, v2

.LBB0_1546:
	v_mov_b32_e32 v3, 0x1000
	v_mov_b32_e32 v4, v119
	v_and_b32_e32 v2, 0xffffff00, v8
	v_mov_b32_e32 v1, 0
	v_add_u32_e32 v2, v2, v0
	ds_write_b32 v1, v2 offset:76
	s_waitcnt vmcnt(0)
	v_add_u32_e32 v11, 0xff, v4
	v_cmp_lt_u32_e32 vcc, s18, v11
	s_and_b64 s[14:15], s[12:13], vcc
	s_andn2_b64 vcc, exec, s[14:15]
	s_cbranch_vccnz .LBB0_1556
	s_movk_i32 s14, 0x1ff
	v_cmp_lt_u32_e32 vcc, s14, v11
	v_lshrrev_b32_e32 v5, 8, v11
	s_cbranch_vccz .LBB0_1551
	v_lshrrev_b32_e32 v0, 6, v2
	v_and_b32_e32 v4, 0xfffffe, v5
	v_lshl_add_u64 v[6:7], s[8:9], 0, v[0:1]
	s_mov_b64 s[14:15], 0x2000
	v_mov_b32_e32 v8, 19
	v_lshl_add_u64 v[6:7], v[6:7], 0, s[14:15]
	v_mov_b32_e32 v9, v8
	v_mov_b32_e32 v0, v4

.LBB0_1556:
	v_mov_b32_e32 v3, v120
	s_movk_i32 s18, 0xff
	v_and_b32_e32 v0, 0xffffff00, v11
	v_add_u32_e32 v0, v0, v2
	ds_write_b32 v1, v0 offset:80
	v_add_u32_e32 v8, 0xff, v3
	v_cmp_lt_u32_e32 vcc, s18, v8
	s_and_b64 s[14:15], s[12:13], vcc
	s_andn2_b64 vcc, exec, s[14:15]
	s_cbranch_vccnz .LBB0_1566
	s_movk_i32 s14, 0x1ff
	v_cmp_lt_u32_e32 vcc, s14, v8
	v_lshrrev_b32_e32 v1, 8, v8
	v_mov_b32_e32 v5, 0
	s_cbranch_vccz .LBB0_1561
	v_lshrrev_b32_e32 v4, 6, v0
	v_and_b32_e32 v2, 0xfffffe, v1
	v_lshl_add_u64 v[4:5], s[8:9], 0, v[4:5]
	s_mov_b64 s[14:15], 0x2000
	v_mov_b32_e32 v6, 20
	v_lshl_add_u64 v[4:5], v[4:5], 0, s[14:15]
	v_mov_b32_e32 v7, v6
	v_mov_b32_e32 v3, v2

.LBB0_1566:
	v_mov_b32_e32 v3, 0x1000
	v_mov_b32_e32 v4, v121
	v_and_b32_e32 v2, 0xffffff00, v8
	v_mov_b32_e32 v1, 0
	v_add_u32_e32 v2, v2, v0
	ds_write_b32 v1, v2 offset:84
	v_add_u32_e32 v11, 0xff, v4
	v_cmp_lt_u32_e32 vcc, s18, v11
	s_and_b64 s[14:15], s[12:13], vcc
	s_andn2_b64 vcc, exec, s[14:15]
	s_cbranch_vccnz .LBB0_1576
	s_movk_i32 s14, 0x1ff
	v_cmp_lt_u32_e32 vcc, s14, v11
	v_lshrrev_b32_e32 v5, 8, v11
	s_cbranch_vccz .LBB0_1571
	v_lshrrev_b32_e32 v0, 6, v2
	v_and_b32_e32 v4, 0xfffffe, v5
	v_lshl_add_u64 v[6:7], s[8:9], 0, v[0:1]
	s_mov_b64 s[14:15], 0x2000
	v_mov_b32_e32 v8, 21
	v_lshl_add_u64 v[6:7], v[6:7], 0, s[14:15]
	v_mov_b32_e32 v9, v8
	v_mov_b32_e32 v0, v4

.LBB0_1576:
	v_mov_b32_e32 v3, v122
	s_movk_i32 s18, 0xff
	v_and_b32_e32 v0, 0xffffff00, v11
	v_add_u32_e32 v0, v0, v2
	ds_write_b32 v1, v0 offset:88
	v_add_u32_e32 v8, 0xff, v3
	v_cmp_lt_u32_e32 vcc, s18, v8
	s_and_b64 s[14:15], s[12:13], vcc
	s_andn2_b64 vcc, exec, s[14:15]
	s_cbranch_vccnz .LBB0_1586
	s_movk_i32 s14, 0x1ff
	v_cmp_lt_u32_e32 vcc, s14, v8
	v_lshrrev_b32_e32 v1, 8, v8
	v_mov_b32_e32 v5, 0
	s_cbranch_vccz .LBB0_1581
	v_lshrrev_b32_e32 v4, 6, v0
	v_and_b32_e32 v2, 0xfffffe, v1
	v_lshl_add_u64 v[4:5], s[8:9], 0, v[4:5]
	s_mov_b64 s[14:15], 0x2000
	v_mov_b32_e32 v6, 22
	v_lshl_add_u64 v[4:5], v[4:5], 0, s[14:15]
	v_mov_b32_e32 v7, v6
	v_mov_b32_e32 v3, v2

.LBB0_1586:
	v_mov_b32_e32 v3, 0x1000
	v_mov_b32_e32 v4, v123
	v_and_b32_e32 v2, 0xffffff00, v8
	v_mov_b32_e32 v1, 0
	v_add_u32_e32 v2, v2, v0
	ds_write_b32 v1, v2 offset:92
	s_waitcnt vmcnt(0)
	v_add_u32_e32 v11, 0xff, v4
	v_cmp_lt_u32_e32 vcc, s18, v11
	s_and_b64 s[14:15], s[12:13], vcc
	s_andn2_b64 vcc, exec, s[14:15]
	s_cbranch_vccnz .LBB0_1596
	s_movk_i32 s14, 0x1ff
	v_cmp_lt_u32_e32 vcc, s14, v11
	v_lshrrev_b32_e32 v5, 8, v11
	s_cbranch_vccz .LBB0_1591
	v_lshrrev_b32_e32 v0, 6, v2
	v_and_b32_e32 v4, 0xfffffe, v5
	v_lshl_add_u64 v[6:7], s[8:9], 0, v[0:1]
	s_mov_b64 s[14:15], 0x2000
	v_mov_b32_e32 v8, 23
	v_lshl_add_u64 v[6:7], v[6:7], 0, s[14:15]
	v_mov_b32_e32 v9, v8
	v_mov_b32_e32 v0, v4

.LBB0_1596:
	v_mov_b32_e32 v3, v124
	s_movk_i32 s18, 0xff
	v_and_b32_e32 v0, 0xffffff00, v11
	v_add_u32_e32 v0, v0, v2
	ds_write_b32 v1, v0 offset:96
	v_add_u32_e32 v8, 0xff, v3
	v_cmp_lt_u32_e32 vcc, s18, v8
	s_and_b64 s[14:15], s[12:13], vcc
	s_andn2_b64 vcc, exec, s[14:15]
	s_cbranch_vccnz .LBB0_1606
	s_movk_i32 s14, 0x1ff
	v_cmp_lt_u32_e32 vcc, s14, v8
	v_lshrrev_b32_e32 v1, 8, v8
	v_mov_b32_e32 v5, 0
	s_cbranch_vccz .LBB0_1601
	v_lshrrev_b32_e32 v4, 6, v0
	v_and_b32_e32 v2, 0xfffffe, v1
	v_lshl_add_u64 v[4:5], s[8:9], 0, v[4:5]
	s_mov_b64 s[14:15], 0x2000
	v_mov_b32_e32 v6, 24
	v_lshl_add_u64 v[4:5], v[4:5], 0, s[14:15]
	v_mov_b32_e32 v7, v6
	v_mov_b32_e32 v3, v2

.LBB0_1606:
	v_mov_b32_e32 v3, 0x1000
	v_mov_b32_e32 v4, v125
	v_and_b32_e32 v2, 0xffffff00, v8
	v_mov_b32_e32 v1, 0
	v_add_u32_e32 v2, v2, v0
	ds_write_b32 v1, v2 offset:100
	v_add_u32_e32 v11, 0xff, v4
	v_cmp_lt_u32_e32 vcc, s18, v11
	s_and_b64 s[14:15], s[12:13], vcc
	s_andn2_b64 vcc, exec, s[14:15]
	s_cbranch_vccnz .LBB0_1616
	s_movk_i32 s14, 0x1ff
	v_cmp_lt_u32_e32 vcc, s14, v11
	v_lshrrev_b32_e32 v5, 8, v11
	s_cbranch_vccz .LBB0_1611
	v_lshrrev_b32_e32 v0, 6, v2
	v_and_b32_e32 v4, 0xfffffe, v5
	v_lshl_add_u64 v[6:7], s[8:9], 0, v[0:1]
	s_mov_b64 s[14:15], 0x2000
	v_mov_b32_e32 v8, 25
	v_lshl_add_u64 v[6:7], v[6:7], 0, s[14:15]
	v_mov_b32_e32 v9, v8
	v_mov_b32_e32 v0, v4

.LBB0_1616:
	v_mov_b32_e32 v3, v126
	s_movk_i32 s18, 0xff
	v_and_b32_e32 v0, 0xffffff00, v11
	v_add_u32_e32 v0, v0, v2
	ds_write_b32 v1, v0 offset:104
	v_add_u32_e32 v8, 0xff, v3
	v_cmp_lt_u32_e32 vcc, s18, v8
	s_and_b64 s[14:15], s[12:13], vcc
	s_andn2_b64 vcc, exec, s[14:15]
	s_cbranch_vccnz .LBB0_1626
	s_movk_i32 s14, 0x1ff
	v_cmp_lt_u32_e32 vcc, s14, v8
	v_lshrrev_b32_e32 v1, 8, v8
	v_mov_b32_e32 v5, 0
	s_cbranch_vccz .LBB0_1621
	v_lshrrev_b32_e32 v4, 6, v0
	v_and_b32_e32 v2, 0xfffffe, v1
	v_lshl_add_u64 v[4:5], s[8:9], 0, v[4:5]
	s_mov_b64 s[14:15], 0x2000
	v_mov_b32_e32 v6, 26
	v_lshl_add_u64 v[4:5], v[4:5], 0, s[14:15]
	v_mov_b32_e32 v7, v6
	v_mov_b32_e32 v3, v2

.LBB0_1626:
	v_mov_b32_e32 v3, 0x1000
	v_mov_b32_e32 v4, v127
	v_and_b32_e32 v2, 0xffffff00, v8
	v_mov_b32_e32 v1, 0
	v_add_u32_e32 v2, v2, v0
	ds_write_b32 v1, v2 offset:108
	s_waitcnt vmcnt(0)
	v_add_u32_e32 v11, 0xff, v4
	v_cmp_lt_u32_e32 vcc, s18, v11
	s_and_b64 s[14:15], s[12:13], vcc
	s_andn2_b64 vcc, exec, s[14:15]
	s_cbranch_vccnz .LBB0_1636
	s_movk_i32 s14, 0x1ff
	v_cmp_lt_u32_e32 vcc, s14, v11
	v_lshrrev_b32_e32 v5, 8, v11
	s_cbranch_vccz .LBB0_1631
	v_lshrrev_b32_e32 v0, 6, v2
	v_and_b32_e32 v4, 0xfffffe, v5
	v_lshl_add_u64 v[6:7], s[8:9], 0, v[0:1]
	s_mov_b64 s[14:15], 0x2000
	v_mov_b32_e32 v8, 27
	v_lshl_add_u64 v[6:7], v[6:7], 0, s[14:15]
	v_mov_b32_e32 v9, v8
	v_mov_b32_e32 v0, v4

.LBB0_1636:
	v_mov_b32_e32 v3, v128
	s_movk_i32 s18, 0xff
	v_and_b32_e32 v0, 0xffffff00, v11
	v_add_u32_e32 v0, v0, v2
	ds_write_b32 v1, v0 offset:112
	v_add_u32_e32 v8, 0xff, v3
	v_cmp_lt_u32_e32 vcc, s18, v8
	s_and_b64 s[14:15], s[12:13], vcc
	s_andn2_b64 vcc, exec, s[14:15]
	s_cbranch_vccnz .LBB0_1646
	s_movk_i32 s14, 0x1ff
	v_cmp_lt_u32_e32 vcc, s14, v8
	v_lshrrev_b32_e32 v1, 8, v8
	v_mov_b32_e32 v5, 0
	s_cbranch_vccz .LBB0_1641
	v_lshrrev_b32_e32 v4, 6, v0
	v_and_b32_e32 v2, 0xfffffe, v1
	v_lshl_add_u64 v[4:5], s[8:9], 0, v[4:5]
	s_mov_b64 s[14:15], 0x2000
	v_mov_b32_e32 v6, 28
	v_lshl_add_u64 v[4:5], v[4:5], 0, s[14:15]
	v_mov_b32_e32 v7, v6
	v_mov_b32_e32 v3, v2

.LBB0_1646:
	v_mov_b32_e32 v3, 0x1000
	v_mov_b32_e32 v4, v129
	v_and_b32_e32 v2, 0xffffff00, v8
	v_mov_b32_e32 v1, 0
	v_add_u32_e32 v2, v2, v0
	ds_write_b32 v1, v2 offset:116
	v_add_u32_e32 v11, 0xff, v4
	v_cmp_lt_u32_e32 vcc, s18, v11
	s_and_b64 s[14:15], s[12:13], vcc
	s_andn2_b64 vcc, exec, s[14:15]
	s_cbranch_vccnz .LBB0_1656
	s_movk_i32 s14, 0x1ff
	v_cmp_lt_u32_e32 vcc, s14, v11
	v_lshrrev_b32_e32 v5, 8, v11
	s_cbranch_vccz .LBB0_1651
	v_lshrrev_b32_e32 v0, 6, v2
	v_and_b32_e32 v4, 0xfffffe, v5
	v_lshl_add_u64 v[6:7], s[8:9], 0, v[0:1]
	s_mov_b64 s[14:15], 0x2000
	v_mov_b32_e32 v8, 29
	v_lshl_add_u64 v[6:7], v[6:7], 0, s[14:15]
	v_mov_b32_e32 v9, v8
	v_mov_b32_e32 v0, v4

.LBB0_1656:
	v_mov_b32_e32 v3, v130
	s_movk_i32 s18, 0xff
	v_and_b32_e32 v0, 0xffffff00, v11
	v_add_u32_e32 v0, v0, v2
	ds_write_b32 v1, v0 offset:120
	v_add_u32_e32 v8, 0xff, v3
	v_cmp_lt_u32_e32 vcc, s18, v8
	s_and_b64 s[14:15], s[12:13], vcc
	s_andn2_b64 vcc, exec, s[14:15]
	s_cbranch_vccnz .LBB0_1666
	s_movk_i32 s14, 0x1ff
	v_cmp_lt_u32_e32 vcc, s14, v8
	v_lshrrev_b32_e32 v1, 8, v8
	v_mov_b32_e32 v5, 0
	s_cbranch_vccz .LBB0_1661
	v_lshrrev_b32_e32 v4, 6, v0
	v_and_b32_e32 v2, 0xfffffe, v1
	v_lshl_add_u64 v[4:5], s[8:9], 0, v[4:5]
	s_mov_b64 s[14:15], 0x2000
	v_mov_b32_e32 v6, 30
	v_lshl_add_u64 v[4:5], v[4:5], 0, s[14:15]
	v_mov_b32_e32 v7, v6
	v_mov_b32_e32 v3, v2

.LBB0_1666:
	v_mov_b32_e32 v1, 0x1000
	v_mov_b32_e32 v1, v131
	v_and_b32_e32 v2, 0xffffff00, v8
	v_mov_b32_e32 v5, 0
	v_add_u32_e32 v0, v2, v0
	ds_write_b32 v5, v0 offset:124
	s_waitcnt vmcnt(0)
	v_add_u32_e32 v1, 0xff, v1
	v_cmp_lt_u32_e32 vcc, s18, v1
	s_and_b64 s[14:15], s[12:13], vcc
	s_andn2_b64 vcc, exec, s[14:15]
	s_cbranch_vccnz .LBB0_1676
	s_movk_i32 s14, 0x1ff
	v_cmp_lt_u32_e32 vcc, s14, v1
	v_lshrrev_b32_e32 v3, 8, v1
	s_cbranch_vccz .LBB0_1671
	v_lshrrev_b32_e32 v4, 6, v0
	v_and_b32_e32 v2, 0xfffffe, v3
	v_lshl_add_u64 v[4:5], s[8:9], 0, v[4:5]
	s_mov_b64 s[14:15], 0x2000
	v_mov_b32_e32 v6, 31
	v_lshl_add_u64 v[4:5], v[4:5], 0, s[14:15]
	v_mov_b32_e32 v7, v6
	v_mov_b32_e32 v8, v2

.LBB0_2476:
	s_add_i32 s42, s34, s39
	s_add_i32 s40, s42, 0xffffff00
	s_cmpk_lt_i32 s42, 0x100
	s_cselect_b32 s41, 0xff, s27
	s_cselect_b32 s43, s42, s40
	s_cselect_b32 s44, s36, s35
	s_add_i32 s45, s41, s38
	s_and_b64 s[40:41], s[12:13], exec
	s_cselect_b32 s40, s43, s45
	s_add_i32 s41, s42, 8
	s_addk_i32 s42, 0xff08
	s_add_i32 s43, s40, s44
	s_cmpk_lt_i32 s41, 0x100
	s_cselect_b32 s40, 0xff, s27
	s_cselect_b32 s42, s41, s42
	s_cselect_b32 s44, s36, s35
	s_add_i32 s38, s38, -8
	s_add_i32 s45, s38, s40
	s_and_b64 s[40:41], s[12:13], exec
	s_waitcnt vmcnt(23)
	v_lshlrev_b32_e32 v1, 16, v48
	s_cselect_b32 s40, s42, s45
	v_and_b32_e32 v48, 0xffff0000, v48
	v_mul_f32_e32 v1, 0x3fb8aa3b, v1
	s_add_i32 s40, s40, s44
	v_lshlrev_b32_e32 v61, 16, v49
	v_and_b32_e32 v49, 0xffff0000, v49
	s_waitcnt vmcnt(8)
	v_lshlrev_b32_e32 v70, 16, v6
	v_and_b32_e32 v71, 0xffff0000, v6
	v_mul_f32_e32 v6, 0x3fb8aa3b, v48
	v_exp_f32_e32 v74, v1
	v_lshl_or_b32 v1, s40, 11, v59
	v_lshlrev_b32_e32 v32, 16, v44
	v_and_b32_e32 v33, 0xffff0000, v44
	v_lshlrev_b32_e32 v34, 16, v45
	v_and_b32_e32 v35, 0xffff0000, v45
	v_lshlrev_b32_e32 v44, 16, v36
	v_and_b32_e32 v36, 0xffff0000, v36
	v_lshlrev_b32_e32 v45, 16, v37
	v_and_b32_e32 v37, 0xffff0000, v37
	v_lshlrev_b32_e32 v38, 16, v30
	v_and_b32_e32 v39, 0xffff0000, v30
	v_lshlrev_b32_e32 v40, 16, v31
	v_and_b32_e32 v41, 0xffff0000, v31
	v_lshlrev_b32_e32 v30, 16, v28
	v_lshlrev_b32_e32 v31, 16, v29
	v_mul_f32_e32 v48, 0x3fb8aa3b, v49
	v_exp_f32_e32 v75, v6
	v_add_u32_e32 v6, s37, v1
	v_lshlrev_b32_e32 v72, 16, v7
	v_and_b32_e32 v73, 0xffff0000, v7
	v_mul_f32_e32 v7, 0x3fb8aa3b, v61
	v_mul_f32_e32 v61, 0x3fb8aa3b, v44
	v_mul_f32_e32 v79, 0x3fb8aa3b, v36
	v_mul_f32_e32 v80, 0x3fb8aa3b, v45
	v_mul_f32_e32 v81, 0x3fb8aa3b, v37
	v_mul_f32_e32 v82, 0x3fb8aa3b, v30
	v_mul_f32_e32 v84, 0x3fb8aa3b, v31
	v_exp_f32_e32 v77, v48
	global_load_dwordx2 v[48:49], v1, s[16:17]
	global_load_dwordx2 v[44:45], v1, s[18:19]
	global_load_dwordx2 v[36:37], v6, s[16:17]
	global_load_dwordx2 v[30:31], v6, s[18:19]
	v_add_u32_e32 v1, s37, v6
	v_and_b32_e32 v28, 0xffff0000, v28
	v_and_b32_e32 v29, 0xffff0000, v29
	v_lshlrev_b32_e32 v42, 16, v26
	v_and_b32_e32 v43, 0xffff0000, v26
	v_lshlrev_b32_e32 v46, 16, v27
	v_and_b32_e32 v47, 0xffff0000, v27
	v_lshlrev_b32_e32 v26, 16, v24
	v_and_b32_e32 v24, 0xffff0000, v24
	v_lshlrev_b32_e32 v27, 16, v25
	v_and_b32_e32 v25, 0xffff0000, v25
	v_lshlrev_b32_e32 v50, 16, v22
	v_and_b32_e32 v51, 0xffff0000, v22
	v_lshlrev_b32_e32 v52, 16, v23
	v_and_b32_e32 v53, 0xffff0000, v23
	v_lshlrev_b32_e32 v22, 16, v20
	v_lshlrev_b32_e32 v23, 16, v21
	v_add_u32_e32 v6, s37, v1
	v_mul_f32_e32 v83, 0x3fb8aa3b, v28
	v_mul_f32_e32 v85, 0x3fb8aa3b, v29
	v_mul_f32_e32 v86, 0x3fb8aa3b, v26
	v_mul_f32_e32 v87, 0x3fb8aa3b, v24
	v_mul_f32_e32 v88, 0x3fb8aa3b, v27
	v_mul_f32_e32 v89, 0x3fb8aa3b, v25
	v_mul_f32_e32 v90, 0x3fb8aa3b, v22
	v_mul_f32_e32 v92, 0x3fb8aa3b, v23
	global_load_dwordx2 v[28:29], v1, s[16:17]
	global_load_dwordx2 v[26:27], v1, s[18:19]
	global_load_dwordx2 v[24:25], v6, s[16:17]
	global_load_dwordx2 v[22:23], v6, s[18:19]
	v_add_u32_e32 v1, s37, v6
	v_and_b32_e32 v20, 0xffff0000, v20
	v_and_b32_e32 v21, 0xffff0000, v21
	v_lshlrev_b32_e32 v54, 16, v18
	v_and_b32_e32 v55, 0xffff0000, v18
	v_lshlrev_b32_e32 v56, 16, v19
	v_and_b32_e32 v57, 0xffff0000, v19
	v_lshlrev_b32_e32 v18, 16, v16
	v_and_b32_e32 v16, 0xffff0000, v16
	v_lshlrev_b32_e32 v19, 16, v17
	v_and_b32_e32 v17, 0xffff0000, v17
	v_lshlrev_b32_e32 v62, 16, v14
	v_and_b32_e32 v63, 0xffff0000, v14
	v_lshlrev_b32_e32 v64, 16, v15
	v_and_b32_e32 v65, 0xffff0000, v15
	v_lshlrev_b32_e32 v14, 16, v12
	v_lshlrev_b32_e32 v15, 16, v13
	v_add_u32_e32 v6, s37, v1
	v_mul_f32_e32 v91, 0x3fb8aa3b, v20
	v_mul_f32_e32 v93, 0x3fb8aa3b, v21
	v_mul_f32_e32 v94, 0x3fb8aa3b, v18
	v_mul_f32_e32 v95, 0x3fb8aa3b, v16
	v_mul_f32_e32 v96, 0x3fb8aa3b, v19
	v_mul_f32_e32 v97, 0x3fb8aa3b, v17
	v_mul_f32_e32 v98, 0x3fb8aa3b, v14
	v_mul_f32_e32 v100, 0x3fb8aa3b, v15
	global_load_dwordx2 v[20:21], v1, s[16:17]
	global_load_dwordx2 v[18:19], v1, s[18:19]
	global_load_dwordx2 v[16:17], v6, s[16:17]
	global_load_dwordx2 v[14:15], v6, s[18:19]
	v_add_u32_e32 v1, s37, v6
	v_and_b32_e32 v12, 0xffff0000, v12
	v_and_b32_e32 v13, 0xffff0000, v13
	v_lshlrev_b32_e32 v66, 16, v10
	v_and_b32_e32 v67, 0xffff0000, v10
	v_lshlrev_b32_e32 v68, 16, v11
	v_and_b32_e32 v69, 0xffff0000, v11
	v_lshlrev_b32_e32 v10, 16, v8
	v_and_b32_e32 v8, 0xffff0000, v8
	v_lshlrev_b32_e32 v11, 16, v9
	v_and_b32_e32 v9, 0xffff0000, v9
	v_add_u32_e32 v6, s37, v1
	v_mul_f32_e32 v99, 0x3fb8aa3b, v12
	v_mul_f32_e32 v101, 0x3fb8aa3b, v13
	v_mul_f32_e32 v102, 0x3fb8aa3b, v10
	v_mul_f32_e32 v103, 0x3fb8aa3b, v8
	v_mul_f32_e32 v104, 0x3fb8aa3b, v11
	v_mul_f32_e32 v105, 0x3fb8aa3b, v9
	v_exp_f32_e32 v76, v7
	global_load_dwordx2 v[12:13], v1, s[16:17]
	global_load_dwordx2 v[10:11], v1, s[18:19]
	global_load_dwordx2 v[8:9], v6, s[16:17]
	s_nop 0
	global_load_dwordx2 v[6:7], v6, s[18:19]
	v_exp_f32_e32 v78, v61
	v_exp_f32_e32 v79, v79
	v_exp_f32_e32 v80, v80
	v_exp_f32_e32 v81, v81
	v_exp_f32_e32 v82, v82
	v_exp_f32_e32 v83, v83
	v_exp_f32_e32 v84, v84
	v_exp_f32_e32 v85, v85
	v_exp_f32_e32 v86, v86
	v_exp_f32_e32 v87, v87
	v_exp_f32_e32 v88, v88
	v_exp_f32_e32 v89, v89
	v_exp_f32_e32 v90, v90
	v_exp_f32_e32 v91, v91
	v_pk_fma_f32 v[2:3], v[2:3], v[74:75], v[32:33]
	v_exp_f32_e32 v92, v92
	v_exp_f32_e32 v93, v93
	v_pk_fma_f32 v[4:5], v[4:5], v[76:77], v[34:35]
	v_cvt_pk_bf16_f32 v32, v2, v3
	v_pk_fma_f32 v[2:3], v[78:79], v[2:3], v[38:39]
	v_exp_f32_e32 v94, v94
	v_exp_f32_e32 v95, v95
	v_exp_f32_e32 v96, v96
	v_exp_f32_e32 v97, v97
	v_cvt_pk_bf16_f32 v33, v4, v5
	v_pk_fma_f32 v[4:5], v[80:81], v[4:5], v[40:41]
	v_cvt_pk_bf16_f32 v34, v2, v3
	v_pk_fma_f32 v[2:3], v[82:83], v[2:3], v[42:43]
	v_lshl_or_b32 v1, s43, 11, v59
	v_exp_f32_e32 v98, v98
	v_exp_f32_e32 v99, v99
	v_exp_f32_e32 v100, v100
	v_exp_f32_e32 v101, v101
	v_cvt_pk_bf16_f32 v35, v4, v5
	v_pk_fma_f32 v[4:5], v[84:85], v[4:5], v[46:47]
	v_cvt_pk_bf16_f32 v38, v2, v3
	v_pk_fma_f32 v[2:3], v[86:87], v[2:3], v[50:51]
	v_add_u32_e32 v61, s37, v1
	v_exp_f32_e32 v102, v102
	v_exp_f32_e32 v103, v103
	v_exp_f32_e32 v104, v104
	v_exp_f32_e32 v105, v105
	v_cvt_pk_bf16_f32 v39, v4, v5
	v_pk_fma_f32 v[4:5], v[88:89], v[4:5], v[52:53]
	v_cvt_pk_bf16_f32 v40, v2, v3
	v_pk_fma_f32 v[2:3], v[90:91], v[2:3], v[54:55]
	v_add_u32_e32 v54, s37, v61
	v_cvt_pk_bf16_f32 v41, v4, v5
	v_pk_fma_f32 v[4:5], v[92:93], v[4:5], v[56:57]
	v_add_u32_e32 v55, s37, v54
	v_cvt_pk_bf16_f32 v42, v2, v3
	v_cvt_pk_bf16_f32 v43, v4, v5
	v_pk_fma_f32 v[4:5], v[96:97], v[4:5], v[64:65]
	v_pk_fma_f32 v[2:3], v[94:95], v[2:3], v[62:63]
	v_add_u32_e32 v56, s37, v55
	v_cvt_pk_bf16_f32 v46, v2, v3
	v_cvt_pk_bf16_f32 v47, v4, v5
	v_pk_fma_f32 v[4:5], v[100:101], v[4:5], v[68:69]
	v_pk_fma_f32 v[2:3], v[98:99], v[2:3], v[66:67]
	s_add_i32 s39, s39, 8
	v_add_u32_e32 v57, s37, v56
	v_cvt_pk_bf16_f32 v50, v2, v3
	v_cvt_pk_bf16_f32 v51, v4, v5
	v_pk_fma_f32 v[4:5], v[104:105], v[4:5], v[72:73]
	v_pk_fma_f32 v[2:3], v[102:103], v[2:3], v[70:71]
	v_add_u32_e32 v62, s37, v57
	s_cmpk_lg_i32 s39, 0x80
	v_cvt_pk_bf16_f32 v52, v2, v3
	v_cvt_pk_bf16_f32 v53, v4, v5
	v_add_u32_e32 v63, s37, v62
	global_store_dwordx2 v1, v[32:33], s[14:15]
	global_store_dwordx2 v61, v[34:35], s[14:15]
	global_store_dwordx2 v54, v[38:39], s[14:15]
	global_store_dwordx2 v55, v[40:41], s[14:15]
	global_store_dwordx2 v56, v[42:43], s[14:15]
	global_store_dwordx2 v57, v[46:47], s[14:15]
	global_store_dwordx2 v62, v[50:51], s[14:15]
	global_store_dwordx2 v63, v[52:53], s[14:15]
	s_cbranch_scc1 .LBB0_2476
	s_waitcnt vmcnt(23)
	v_lshlrev_b32_e32 v1, 16, v48
	v_and_b32_e32 v35, 0xffff0000, v48
	v_lshlrev_b32_e32 v38, 16, v49
	v_mul_f32_e32 v1, 0x3fb8aa3b, v1
	v_and_b32_e32 v39, 0xffff0000, v49
	v_exp_f32_e32 v34, v1
	v_mul_f32_e32 v1, 0x3fb8aa3b, v35
	v_mul_f32_e32 v35, 0x3fb8aa3b, v38
	v_exp_f32_e32 v38, v35
	v_mul_f32_e32 v35, 0x3fb8aa3b, v39
	v_exp_f32_e32 v39, v35
	v_exp_f32_e32 v35, v1
	s_waitcnt vmcnt(22)
	v_lshlrev_b32_e32 v40, 16, v45
	v_and_b32_e32 v41, 0xffff0000, v45
	s_waitcnt vmcnt(21)
	v_lshlrev_b32_e32 v1, 16, v36
	v_lshlrev_b32_e32 v32, 16, v44
	v_and_b32_e32 v33, 0xffff0000, v44
	v_pk_fma_f32 v[4:5], v[38:39], v[4:5], v[40:41]
	v_and_b32_e32 v38, 0xffff0000, v36
	v_lshlrev_b32_e32 v39, 16, v37
	v_mul_f32_e32 v1, 0x3fb8aa3b, v1
	v_pk_fma_f32 v[2:3], v[34:35], v[2:3], v[32:33]
	v_and_b32_e32 v37, 0xffff0000, v37
	s_waitcnt vmcnt(20)
	v_lshlrev_b32_e32 v34, 16, v30
	v_and_b32_e32 v35, 0xffff0000, v30
	v_exp_f32_e32 v36, v1
	v_mul_f32_e32 v1, 0x3fb8aa3b, v38
	v_mul_f32_e32 v30, 0x3fb8aa3b, v39
	v_exp_f32_e32 v38, v30
	v_mul_f32_e32 v30, 0x3fb8aa3b, v37
	v_exp_f32_e32 v37, v1
	s_waitcnt vmcnt(19)
	v_lshlrev_b32_e32 v1, 16, v28
	v_cvt_pk_bf16_f32 v32, v2, v3
	v_mul_f32_e32 v1, 0x3fb8aa3b, v1
	v_pk_fma_f32 v[2:3], v[36:37], v[2:3], v[34:35]
	v_and_b32_e32 v35, 0xffff0000, v28
	v_exp_f32_e32 v34, v1
	v_mul_f32_e32 v1, 0x3fb8aa3b, v35
	v_exp_f32_e32 v39, v30
	v_exp_f32_e32 v35, v1
	v_lshlrev_b32_e32 v30, 16, v31
	v_and_b32_e32 v31, 0xffff0000, v31
	v_lshlrev_b32_e32 v36, 16, v29
	v_and_b32_e32 v37, 0xffff0000, v29
	s_waitcnt vmcnt(18)
	v_lshlrev_b32_e32 v28, 16, v26
	v_and_b32_e32 v29, 0xffff0000, v26
	s_waitcnt vmcnt(17)
	v_lshlrev_b32_e32 v1, 16, v24
	v_cvt_pk_bf16_f32 v33, v4, v5
	v_pk_fma_f32 v[4:5], v[38:39], v[4:5], v[30:31]
	v_cvt_pk_bf16_f32 v30, v2, v3
	v_mul_f32_e32 v26, 0x3fb8aa3b, v36
	v_pk_fma_f32 v[2:3], v[34:35], v[2:3], v[28:29]
	v_and_b32_e32 v29, 0xffff0000, v24
	v_mul_f32_e32 v1, 0x3fb8aa3b, v1
	v_exp_f32_e32 v36, v26
	v_mul_f32_e32 v26, 0x3fb8aa3b, v37
	v_exp_f32_e32 v28, v1
	v_mul_f32_e32 v1, 0x3fb8aa3b, v29
	v_exp_f32_e32 v37, v26
	v_exp_f32_e32 v29, v1
	v_lshlrev_b32_e32 v26, 16, v27
	v_and_b32_e32 v27, 0xffff0000, v27
	v_lshlrev_b32_e32 v34, 16, v25
	v_and_b32_e32 v35, 0xffff0000, v25
	s_waitcnt vmcnt(16)
	v_lshlrev_b32_e32 v24, 16, v22
	v_and_b32_e32 v25, 0xffff0000, v22
	s_waitcnt vmcnt(15)
	v_lshlrev_b32_e32 v1, 16, v20
	v_cvt_pk_bf16_f32 v31, v4, v5
	v_pk_fma_f32 v[4:5], v[36:37], v[4:5], v[26:27]
	v_cvt_pk_bf16_f32 v26, v2, v3
	v_mul_f32_e32 v22, 0x3fb8aa3b, v34
	v_pk_fma_f32 v[2:3], v[28:29], v[2:3], v[24:25]
	v_and_b32_e32 v25, 0xffff0000, v20
	v_mul_f32_e32 v1, 0x3fb8aa3b, v1
	v_exp_f32_e32 v34, v22
	v_mul_f32_e32 v22, 0x3fb8aa3b, v35
	v_exp_f32_e32 v24, v1
	v_mul_f32_e32 v1, 0x3fb8aa3b, v25
	v_exp_f32_e32 v35, v22
	v_exp_f32_e32 v25, v1
	v_lshlrev_b32_e32 v22, 16, v23
	v_and_b32_e32 v23, 0xffff0000, v23
	v_lshlrev_b32_e32 v28, 16, v21
	v_and_b32_e32 v29, 0xffff0000, v21
	s_waitcnt vmcnt(14)
	v_lshlrev_b32_e32 v20, 16, v18
	v_and_b32_e32 v21, 0xffff0000, v18
	s_waitcnt vmcnt(13)
	v_lshlrev_b32_e32 v1, 16, v16
	v_cvt_pk_bf16_f32 v27, v4, v5
	v_pk_fma_f32 v[4:5], v[34:35], v[4:5], v[22:23]
	v_cvt_pk_bf16_f32 v22, v2, v3
	v_mul_f32_e32 v18, 0x3fb8aa3b, v28
	v_pk_fma_f32 v[2:3], v[24:25], v[2:3], v[20:21]
	v_and_b32_e32 v21, 0xffff0000, v16
	v_mul_f32_e32 v1, 0x3fb8aa3b, v1
	v_exp_f32_e32 v28, v18
	v_mul_f32_e32 v18, 0x3fb8aa3b, v29
	v_exp_f32_e32 v20, v1
	v_mul_f32_e32 v1, 0x3fb8aa3b, v21
	v_exp_f32_e32 v29, v18
	v_exp_f32_e32 v21, v1
	v_lshlrev_b32_e32 v18, 16, v19
	v_and_b32_e32 v19, 0xffff0000, v19
	v_lshlrev_b32_e32 v24, 16, v17
	v_and_b32_e32 v25, 0xffff0000, v17
	s_waitcnt vmcnt(12)
	v_lshlrev_b32_e32 v16, 16, v14
	v_and_b32_e32 v17, 0xffff0000, v14
	s_waitcnt vmcnt(11)
	v_lshlrev_b32_e32 v1, 16, v12
	v_cvt_pk_bf16_f32 v23, v4, v5
	v_pk_fma_f32 v[4:5], v[28:29], v[4:5], v[18:19]
	v_cvt_pk_bf16_f32 v18, v2, v3
	v_mul_f32_e32 v14, 0x3fb8aa3b, v24
	v_pk_fma_f32 v[2:3], v[20:21], v[2:3], v[16:17]
	v_and_b32_e32 v17, 0xffff0000, v12
	v_mul_f32_e32 v1, 0x3fb8aa3b, v1
	v_exp_f32_e32 v24, v14
	v_mul_f32_e32 v14, 0x3fb8aa3b, v25
	v_exp_f32_e32 v16, v1
	v_mul_f32_e32 v1, 0x3fb8aa3b, v17
	v_exp_f32_e32 v25, v14
	v_exp_f32_e32 v17, v1
	s_cmp_lt_i32 s33, 1
	s_cselect_b32 s16, 0x80, s29
	s_cselect_b32 s17, s30, 0x107f
	s_cselect_b32 s18, s36, s35
	s_add_i32 s16, s16, s34
	s_sub_i32 s17, s17, s34
	v_lshlrev_b32_e32 v14, 16, v15
	v_and_b32_e32 v15, 0xffff0000, v15
	v_lshlrev_b32_e32 v20, 16, v13
	v_and_b32_e32 v21, 0xffff0000, v13
	s_waitcnt vmcnt(10)
	v_lshlrev_b32_e32 v12, 16, v10
	v_and_b32_e32 v13, 0xffff0000, v10
	s_waitcnt vmcnt(9)
	v_lshlrev_b32_e32 v1, 16, v8
	s_and_b64 s[12:13], s[12:13], exec
	v_cvt_pk_bf16_f32 v19, v4, v5
	v_pk_fma_f32 v[4:5], v[24:25], v[4:5], v[14:15]
	v_cvt_pk_bf16_f32 v14, v2, v3
	v_pk_fma_f32 v[2:3], v[16:17], v[2:3], v[12:13]
	v_and_b32_e32 v13, 0xffff0000, v8
	v_mul_f32_e32 v1, 0x3fb8aa3b, v1
	s_cselect_b32 s12, s16, s17
	v_mul_f32_e32 v10, 0x3fb8aa3b, v20
	v_lshlrev_b32_e32 v16, 16, v9
	v_exp_f32_e32 v12, v1
	v_mul_f32_e32 v1, 0x3fb8aa3b, v13
	s_add_i32 s18, s18, s12
	v_exp_f32_e32 v20, v10
	v_mul_f32_e32 v10, 0x3fb8aa3b, v21
	v_and_b32_e32 v17, 0xffff0000, v9
	s_waitcnt vmcnt(8)
	v_lshlrev_b32_e32 v8, 16, v6
	v_and_b32_e32 v9, 0xffff0000, v6
	v_mul_f32_e32 v6, 0x3fb8aa3b, v16
	v_exp_f32_e32 v13, v1
	v_lshl_or_b32 v1, s18, 11, v59
	v_exp_f32_e32 v21, v10
	v_exp_f32_e32 v16, v6
	v_mul_f32_e32 v6, 0x3fb8aa3b, v17
	global_store_dwordx2 v1, v[32:33], s[14:15]
	v_add_u32_e32 v1, s37, v1
	v_exp_f32_e32 v17, v6
	global_store_dwordx2 v1, v[30:31], s[14:15]
	v_add_u32_e32 v1, s37, v1
	global_store_dwordx2 v1, v[26:27], s[14:15]
	v_add_u32_e32 v1, s37, v1
	v_lshlrev_b32_e32 v10, 16, v11
	v_and_b32_e32 v11, 0xffff0000, v11
	global_store_dwordx2 v1, v[22:23], s[14:15]
	v_add_u32_e32 v1, s37, v1
	v_cvt_pk_bf16_f32 v15, v4, v5
	v_pk_fma_f32 v[4:5], v[20:21], v[4:5], v[10:11]
	v_lshlrev_b32_e32 v6, 16, v7
	v_and_b32_e32 v7, 0xffff0000, v7
	global_store_dwordx2 v1, v[18:19], s[14:15]
	v_add_u32_e32 v1, s37, v1
	v_add_u32_e32 v58, s20, v58
	v_cvt_pk_bf16_f32 v10, v2, v3
	v_cvt_pk_bf16_f32 v11, v4, v5
	v_pk_fma_f32 v[4:5], v[16:17], v[4:5], v[6:7]
	v_pk_fma_f32 v[2:3], v[12:13], v[2:3], v[8:9]
	global_store_dwordx2 v1, v[14:15], s[14:15]
	v_add_u32_e32 v1, s37, v1
	v_cmp_lt_i32_e32 vcc, s31, v58
	v_cvt_pk_bf16_f32 v2, v2, v3
	v_cvt_pk_bf16_f32 v3, v4, v5
	global_store_dwordx2 v1, v[10:11], s[14:15]
	v_add_u32_e32 v1, s37, v1
	s_or_b64 s[10:11], vcc, s[10:11]
	global_store_dwordx2 v1, v[2:3], s[14:15]
	s_andn2_b64 exec, exec, s[10:11]
	s_cbranch_execnz .LBB0_2467

.LBB0_3172:
	s_cmp_lt_i32 s88, 29
	s_cselect_b64 s[2:3], -1, 0
	s_and_b64 s[4:5], s[2:3], s[4:5]
	s_andn2_b64 vcc, exec, s[4:5]
	s_cbranch_vccnz .LBB0_3510
	v_mbcnt_lo_u32_b32 v0, -1, 0
	v_mbcnt_hi_u32_b32 v0, -1, v0
	s_mov_b64 s[8:9], s[86:87]
	s_waitcnt vmcnt(0)
	v_lshl_or_b32 v10, s96, 6, v0
	v_readlane_b32 s4, v254, 0
	s_load_dword s5, s[0:1], 0x108
	s_add_u32 s6, s8, 0x1080
	s_addc_u32 s7, s9, 0
	v_cmp_eq_u32_e32 vcc, 0, v10
	s_and_saveexec_b64 s[10:11], vcc
	s_cbranch_execz .LBB0_3494
	v_mov_b32_e32 v4, 0
	global_load_dwordx4 v[100:103], v4, s[6:7] sc1
	global_load_dwordx4 v[104:107], v4, s[6:7] offset:16 sc1
	global_load_dwordx4 v[108:111], v4, s[6:7] offset:32 sc1
	global_load_dwordx4 v[112:115], v4, s[6:7] offset:48 sc1
	global_load_dwordx4 v[116:119], v4, s[6:7] offset:64 sc1
	global_load_dwordx4 v[120:123], v4, s[6:7] offset:80 sc1
	global_load_dwordx4 v[124:127], v4, s[6:7] offset:96 sc1
	global_load_dwordx4 v[128:131], v4, s[6:7] offset:112 sc1
	s_waitcnt vmcnt(0)
	v_mov_b32_e32 v0, v100
	v_mov_b32_e32 v1, 0
	s_cmp_eq_u32 s4, 0
	s_movk_i32 s16, 0xff
	ds_write_b32 v4, v1
	s_cselect_b64 s[12:13], -1, 0
	v_add_u32_e32 v1, 0xff, v0
	v_cmp_lt_u32_e32 vcc, s16, v1
	s_and_b64 s[14:15], s[12:13], vcc
	s_andn2_b64 vcc, exec, s[14:15]
	v_lshrrev_b32_e32 v0, 8, v1
	s_cbranch_vccnz .LBB0_3182
	s_movk_i32 s14, 0x200
	v_cmp_gt_u32_e32 vcc, s14, v1
	s_mov_b64 s[14:15], -1
	s_cbranch_vccnz .LBB0_3179
	s_add_u32 s14, s8, 0x3000
	v_and_b32_e32 v4, 0xfffffe, v0
	v_mov_b32_e32 v2, 0
	s_addc_u32 s15, s9, 0
	v_mov_b32_e32 v3, v2
	v_mov_b32_e32 v5, v4

.LBB0_3182:
	v_mov_b32_e32 v11, 0x1000
	v_mov_b32_e32 v2, v101
	v_and_b32_e32 v9, 0xffffff00, v1
	v_mov_b32_e32 v8, 0
	ds_write_b32 v8, v9 offset:4
	v_add_u32_e32 v12, 0xff, v2
	v_cmp_lt_u32_e32 vcc, s16, v12
	s_and_b64 s[14:15], s[12:13], vcc
	s_andn2_b64 vcc, exec, s[14:15]
	s_cbranch_vccnz .LBB0_3192
	s_movk_i32 s14, 0x1ff
	v_cmp_lt_u32_e32 vcc, s14, v12
	v_lshrrev_b32_e32 v3, 8, v12
	s_cbranch_vccz .LBB0_3187
	v_mov_b32_e32 v1, 0
	v_lshlrev_b32_e32 v4, 2, v0
	v_mov_b32_e32 v5, v1
	v_and_b32_e32 v2, 0xfffffe, v3
	v_lshl_add_u64 v[4:5], s[8:9], 0, v[4:5]
	s_mov_b64 s[14:15], 0x3000
	v_mov_b32_e32 v6, 1
	v_lshl_add_u64 v[4:5], v[4:5], 0, s[14:15]
	v_mov_b32_e32 v7, v6
	v_mov_b32_e32 v13, v2

.LBB0_3192:
	v_mov_b32_e32 v1, v102
	s_movk_i32 s18, 0xff
	v_and_b32_e32 v0, 0xffffff00, v12
	v_add_u32_e32 v0, v0, v9
	ds_write_b32 v8, v0 offset:8
	v_add_u32_e32 v1, 0xff, v1
	v_cmp_lt_u32_e32 vcc, s18, v1
	s_and_b64 s[14:15], s[12:13], vcc
	s_andn2_b64 vcc, exec, s[14:15]
	s_cbranch_vccnz .LBB0_3202
	s_movk_i32 s14, 0x1ff
	v_cmp_lt_u32_e32 vcc, s14, v1
	v_lshrrev_b32_e32 v3, 8, v1
	v_mov_b32_e32 v5, 0
	s_cbranch_vccz .LBB0_3197
	v_lshrrev_b32_e32 v4, 6, v0
	v_and_b32_e32 v2, 0xfffffe, v3
	v_lshl_add_u64 v[4:5], s[8:9], 0, v[4:5]
	s_mov_b64 s[14:15], 0x3000
	v_mov_b32_e32 v6, 2
	v_lshl_add_u64 v[4:5], v[4:5], 0, s[14:15]
	v_mov_b32_e32 v7, v6
	v_mov_b32_e32 v8, v2

.LBB0_3202:
	v_mov_b32_e32 v3, 0x1000
	v_mov_b32_e32 v4, v103
	v_and_b32_e32 v2, 0xffffff00, v1
	v_mov_b32_e32 v1, 0
	v_add_u32_e32 v2, v2, v0
	ds_write_b32 v1, v2 offset:12
	s_waitcnt vmcnt(0)
	v_add_u32_e32 v11, 0xff, v4
	v_cmp_lt_u32_e32 vcc, s18, v11
	s_and_b64 s[14:15], s[12:13], vcc
	s_andn2_b64 vcc, exec, s[14:15]
	s_cbranch_vccnz .LBB0_3212
	s_movk_i32 s14, 0x1ff
	v_cmp_lt_u32_e32 vcc, s14, v11
	v_lshrrev_b32_e32 v5, 8, v11
	s_cbranch_vccz .LBB0_3207
	v_lshrrev_b32_e32 v0, 6, v2
	v_and_b32_e32 v4, 0xfffffe, v5
	v_lshl_add_u64 v[6:7], s[8:9], 0, v[0:1]
	s_mov_b64 s[14:15], 0x3000
	v_mov_b32_e32 v8, 3
	v_lshl_add_u64 v[6:7], v[6:7], 0, s[14:15]
	v_mov_b32_e32 v9, v8
	v_mov_b32_e32 v0, v4

.LBB0_3212:
	v_mov_b32_e32 v3, v104
	s_movk_i32 s18, 0xff
	v_and_b32_e32 v0, 0xffffff00, v11
	v_add_u32_e32 v0, v0, v2
	ds_write_b32 v1, v0 offset:16
	v_add_u32_e32 v8, 0xff, v3
	v_cmp_lt_u32_e32 vcc, s18, v8
	s_and_b64 s[14:15], s[12:13], vcc
	s_andn2_b64 vcc, exec, s[14:15]
	s_cbranch_vccnz .LBB0_3222
	s_movk_i32 s14, 0x1ff
	v_cmp_lt_u32_e32 vcc, s14, v8
	v_lshrrev_b32_e32 v1, 8, v8
	v_mov_b32_e32 v5, 0
	s_cbranch_vccz .LBB0_3217
	v_lshrrev_b32_e32 v4, 6, v0
	v_and_b32_e32 v2, 0xfffffe, v1
	v_lshl_add_u64 v[4:5], s[8:9], 0, v[4:5]
	s_mov_b64 s[14:15], 0x3000
	v_mov_b32_e32 v6, 4
	v_lshl_add_u64 v[4:5], v[4:5], 0, s[14:15]
	v_mov_b32_e32 v7, v6
	v_mov_b32_e32 v3, v2

.LBB0_3222:
	v_mov_b32_e32 v3, 0x1000
	v_mov_b32_e32 v4, v105
	v_and_b32_e32 v2, 0xffffff00, v8
	v_mov_b32_e32 v1, 0
	v_add_u32_e32 v2, v2, v0
	ds_write_b32 v1, v2 offset:20
	v_add_u32_e32 v11, 0xff, v4
	v_cmp_lt_u32_e32 vcc, s18, v11
	s_and_b64 s[14:15], s[12:13], vcc
	s_andn2_b64 vcc, exec, s[14:15]
	s_cbranch_vccnz .LBB0_3232
	s_movk_i32 s14, 0x1ff
	v_cmp_lt_u32_e32 vcc, s14, v11
	v_lshrrev_b32_e32 v5, 8, v11
	s_cbranch_vccz .LBB0_3227
	v_lshrrev_b32_e32 v0, 6, v2
	v_and_b32_e32 v4, 0xfffffe, v5
	v_lshl_add_u64 v[6:7], s[8:9], 0, v[0:1]
	s_mov_b64 s[14:15], 0x3000
	v_mov_b32_e32 v8, 5
	v_lshl_add_u64 v[6:7], v[6:7], 0, s[14:15]
	v_mov_b32_e32 v9, v8
	v_mov_b32_e32 v0, v4

.LBB0_3232:
	v_mov_b32_e32 v3, v106
	s_movk_i32 s18, 0xff
	v_and_b32_e32 v0, 0xffffff00, v11
	v_add_u32_e32 v0, v0, v2
	ds_write_b32 v1, v0 offset:24
	v_add_u32_e32 v8, 0xff, v3
	v_cmp_lt_u32_e32 vcc, s18, v8
	s_and_b64 s[14:15], s[12:13], vcc
	s_andn2_b64 vcc, exec, s[14:15]
	s_cbranch_vccnz .LBB0_3242
	s_movk_i32 s14, 0x1ff
	v_cmp_lt_u32_e32 vcc, s14, v8
	v_lshrrev_b32_e32 v1, 8, v8
	v_mov_b32_e32 v5, 0
	s_cbranch_vccz .LBB0_3237
	v_lshrrev_b32_e32 v4, 6, v0
	v_and_b32_e32 v2, 0xfffffe, v1
	v_lshl_add_u64 v[4:5], s[8:9], 0, v[4:5]
	s_mov_b64 s[14:15], 0x3000
	v_mov_b32_e32 v6, 6
	v_lshl_add_u64 v[4:5], v[4:5], 0, s[14:15]
	v_mov_b32_e32 v7, v6
	v_mov_b32_e32 v3, v2

.LBB0_3242:
	v_mov_b32_e32 v3, 0x1000
	v_mov_b32_e32 v4, v107
	v_and_b32_e32 v2, 0xffffff00, v8
	v_mov_b32_e32 v1, 0
	v_add_u32_e32 v2, v2, v0
	ds_write_b32 v1, v2 offset:28
	s_waitcnt vmcnt(0)
	v_add_u32_e32 v11, 0xff, v4
	v_cmp_lt_u32_e32 vcc, s18, v11
	s_and_b64 s[14:15], s[12:13], vcc
	s_andn2_b64 vcc, exec, s[14:15]
	s_cbranch_vccnz .LBB0_3252
	s_movk_i32 s14, 0x1ff
	v_cmp_lt_u32_e32 vcc, s14, v11
	v_lshrrev_b32_e32 v5, 8, v11
	s_cbranch_vccz .LBB0_3247
	v_lshrrev_b32_e32 v0, 6, v2
	v_and_b32_e32 v4, 0xfffffe, v5
	v_lshl_add_u64 v[6:7], s[8:9], 0, v[0:1]
	s_mov_b64 s[14:15], 0x3000
	v_mov_b32_e32 v8, 7
	v_lshl_add_u64 v[6:7], v[6:7], 0, s[14:15]
	v_mov_b32_e32 v9, v8
	v_mov_b32_e32 v0, v4

.LBB0_3252:
	v_mov_b32_e32 v3, v108
	s_movk_i32 s18, 0xff
	v_and_b32_e32 v0, 0xffffff00, v11
	v_add_u32_e32 v0, v0, v2
	ds_write_b32 v1, v0 offset:32
	v_add_u32_e32 v8, 0xff, v3
	v_cmp_lt_u32_e32 vcc, s18, v8
	s_and_b64 s[14:15], s[12:13], vcc
	s_andn2_b64 vcc, exec, s[14:15]
	s_cbranch_vccnz .LBB0_3262
	s_movk_i32 s14, 0x1ff
	v_cmp_lt_u32_e32 vcc, s14, v8
	v_lshrrev_b32_e32 v1, 8, v8
	v_mov_b32_e32 v5, 0
	s_cbranch_vccz .LBB0_3257
	v_lshrrev_b32_e32 v4, 6, v0
	v_and_b32_e32 v2, 0xfffffe, v1
	v_lshl_add_u64 v[4:5], s[8:9], 0, v[4:5]
	s_mov_b64 s[14:15], 0x3000
	v_mov_b32_e32 v6, 8
	v_lshl_add_u64 v[4:5], v[4:5], 0, s[14:15]
	v_mov_b32_e32 v7, v6
	v_mov_b32_e32 v3, v2

.LBB0_3262:
	v_mov_b32_e32 v3, 0x1000
	v_mov_b32_e32 v4, v109
	v_and_b32_e32 v2, 0xffffff00, v8
	v_mov_b32_e32 v1, 0
	v_add_u32_e32 v2, v2, v0
	ds_write_b32 v1, v2 offset:36
	v_add_u32_e32 v11, 0xff, v4
	v_cmp_lt_u32_e32 vcc, s18, v11
	s_and_b64 s[14:15], s[12:13], vcc
	s_andn2_b64 vcc, exec, s[14:15]
	s_cbranch_vccnz .LBB0_3272
	s_movk_i32 s14, 0x1ff
	v_cmp_lt_u32_e32 vcc, s14, v11
	v_lshrrev_b32_e32 v5, 8, v11
	s_cbranch_vccz .LBB0_3267
	v_lshrrev_b32_e32 v0, 6, v2
	v_and_b32_e32 v4, 0xfffffe, v5
	v_lshl_add_u64 v[6:7], s[8:9], 0, v[0:1]
	s_mov_b64 s[14:15], 0x3000
	v_mov_b32_e32 v8, 9
	v_lshl_add_u64 v[6:7], v[6:7], 0, s[14:15]
	v_mov_b32_e32 v9, v8
	v_mov_b32_e32 v0, v4

.LBB0_3272:
	v_mov_b32_e32 v3, v110
	s_movk_i32 s18, 0xff
	v_and_b32_e32 v0, 0xffffff00, v11
	v_add_u32_e32 v0, v0, v2
	ds_write_b32 v1, v0 offset:40
	v_add_u32_e32 v8, 0xff, v3
	v_cmp_lt_u32_e32 vcc, s18, v8
	s_and_b64 s[14:15], s[12:13], vcc
	s_andn2_b64 vcc, exec, s[14:15]
	s_cbranch_vccnz .LBB0_3282
	s_movk_i32 s14, 0x1ff
	v_cmp_lt_u32_e32 vcc, s14, v8
	v_lshrrev_b32_e32 v1, 8, v8
	v_mov_b32_e32 v5, 0
	s_cbranch_vccz .LBB0_3277
	v_lshrrev_b32_e32 v4, 6, v0
	v_and_b32_e32 v2, 0xfffffe, v1
	v_lshl_add_u64 v[4:5], s[8:9], 0, v[4:5]
	s_mov_b64 s[14:15], 0x3000
	v_mov_b32_e32 v6, 10
	v_lshl_add_u64 v[4:5], v[4:5], 0, s[14:15]
	v_mov_b32_e32 v7, v6
	v_mov_b32_e32 v3, v2

.LBB0_3282:
	v_mov_b32_e32 v3, 0x1000
	v_mov_b32_e32 v4, v111
	v_and_b32_e32 v2, 0xffffff00, v8
	v_mov_b32_e32 v1, 0
	v_add_u32_e32 v2, v2, v0
	ds_write_b32 v1, v2 offset:44
	s_waitcnt vmcnt(0)
	v_add_u32_e32 v11, 0xff, v4
	v_cmp_lt_u32_e32 vcc, s18, v11
	s_and_b64 s[14:15], s[12:13], vcc
	s_andn2_b64 vcc, exec, s[14:15]
	s_cbranch_vccnz .LBB0_3292
	s_movk_i32 s14, 0x1ff
	v_cmp_lt_u32_e32 vcc, s14, v11
	v_lshrrev_b32_e32 v5, 8, v11
	s_cbranch_vccz .LBB0_3287
	v_lshrrev_b32_e32 v0, 6, v2
	v_and_b32_e32 v4, 0xfffffe, v5
	v_lshl_add_u64 v[6:7], s[8:9], 0, v[0:1]
	s_mov_b64 s[14:15], 0x3000
	v_mov_b32_e32 v8, 11
	v_lshl_add_u64 v[6:7], v[6:7], 0, s[14:15]
	v_mov_b32_e32 v9, v8
	v_mov_b32_e32 v0, v4

.LBB0_3292:
	v_mov_b32_e32 v3, v112
	s_movk_i32 s18, 0xff
	v_and_b32_e32 v0, 0xffffff00, v11
	v_add_u32_e32 v0, v0, v2
	ds_write_b32 v1, v0 offset:48
	v_add_u32_e32 v8, 0xff, v3
	v_cmp_lt_u32_e32 vcc, s18, v8
	s_and_b64 s[14:15], s[12:13], vcc
	s_andn2_b64 vcc, exec, s[14:15]
	s_cbranch_vccnz .LBB0_3302
	s_movk_i32 s14, 0x1ff
	v_cmp_lt_u32_e32 vcc, s14, v8
	v_lshrrev_b32_e32 v1, 8, v8
	v_mov_b32_e32 v5, 0
	s_cbranch_vccz .LBB0_3297
	v_lshrrev_b32_e32 v4, 6, v0
	v_and_b32_e32 v2, 0xfffffe, v1
	v_lshl_add_u64 v[4:5], s[8:9], 0, v[4:5]
	s_mov_b64 s[14:15], 0x3000
	v_mov_b32_e32 v6, 12
	v_lshl_add_u64 v[4:5], v[4:5], 0, s[14:15]
	v_mov_b32_e32 v7, v6
	v_mov_b32_e32 v3, v2

.LBB0_3302:
	v_mov_b32_e32 v3, 0x1000
	v_mov_b32_e32 v4, v113
	v_and_b32_e32 v2, 0xffffff00, v8
	v_mov_b32_e32 v1, 0
	v_add_u32_e32 v2, v2, v0
	ds_write_b32 v1, v2 offset:52
	v_add_u32_e32 v11, 0xff, v4
	v_cmp_lt_u32_e32 vcc, s18, v11
	s_and_b64 s[14:15], s[12:13], vcc
	s_andn2_b64 vcc, exec, s[14:15]
	s_cbranch_vccnz .LBB0_3312
	s_movk_i32 s14, 0x1ff
	v_cmp_lt_u32_e32 vcc, s14, v11
	v_lshrrev_b32_e32 v5, 8, v11
	s_cbranch_vccz .LBB0_3307
	v_lshrrev_b32_e32 v0, 6, v2
	v_and_b32_e32 v4, 0xfffffe, v5
	v_lshl_add_u64 v[6:7], s[8:9], 0, v[0:1]
	s_mov_b64 s[14:15], 0x3000
	v_mov_b32_e32 v8, 13
	v_lshl_add_u64 v[6:7], v[6:7], 0, s[14:15]
	v_mov_b32_e32 v9, v8
	v_mov_b32_e32 v0, v4

.LBB0_3312:
	v_mov_b32_e32 v3, v114
	s_movk_i32 s18, 0xff
	v_and_b32_e32 v0, 0xffffff00, v11
	v_add_u32_e32 v0, v0, v2
	ds_write_b32 v1, v0 offset:56
	v_add_u32_e32 v8, 0xff, v3
	v_cmp_lt_u32_e32 vcc, s18, v8
	s_and_b64 s[14:15], s[12:13], vcc
	s_andn2_b64 vcc, exec, s[14:15]
	s_cbranch_vccnz .LBB0_3322
	s_movk_i32 s14, 0x1ff
	v_cmp_lt_u32_e32 vcc, s14, v8
	v_lshrrev_b32_e32 v1, 8, v8
	v_mov_b32_e32 v5, 0
	s_cbranch_vccz .LBB0_3317
	v_lshrrev_b32_e32 v4, 6, v0
	v_and_b32_e32 v2, 0xfffffe, v1
	v_lshl_add_u64 v[4:5], s[8:9], 0, v[4:5]
	s_mov_b64 s[14:15], 0x3000
	v_mov_b32_e32 v6, 14
	v_lshl_add_u64 v[4:5], v[4:5], 0, s[14:15]
	v_mov_b32_e32 v7, v6
	v_mov_b32_e32 v3, v2

.LBB0_3322:
	v_mov_b32_e32 v3, 0x1000
	v_mov_b32_e32 v4, v115
	v_and_b32_e32 v2, 0xffffff00, v8
	v_mov_b32_e32 v1, 0
	v_add_u32_e32 v2, v2, v0
	ds_write_b32 v1, v2 offset:60
	s_waitcnt vmcnt(0)
	v_add_u32_e32 v11, 0xff, v4
	v_cmp_lt_u32_e32 vcc, s18, v11
	s_and_b64 s[14:15], s[12:13], vcc
	s_andn2_b64 vcc, exec, s[14:15]
	s_cbranch_vccnz .LBB0_3332
	s_movk_i32 s14, 0x1ff
	v_cmp_lt_u32_e32 vcc, s14, v11
	v_lshrrev_b32_e32 v5, 8, v11
	s_cbranch_vccz .LBB0_3327
	v_lshrrev_b32_e32 v0, 6, v2
	v_and_b32_e32 v4, 0xfffffe, v5
	v_lshl_add_u64 v[6:7], s[8:9], 0, v[0:1]
	s_mov_b64 s[14:15], 0x3000
	v_mov_b32_e32 v8, 15
	v_lshl_add_u64 v[6:7], v[6:7], 0, s[14:15]
	v_mov_b32_e32 v9, v8
	v_mov_b32_e32 v0, v4

.LBB0_3332:
	v_mov_b32_e32 v3, v116
	s_movk_i32 s18, 0xff
	v_and_b32_e32 v0, 0xffffff00, v11
	v_add_u32_e32 v0, v0, v2
	ds_write_b32 v1, v0 offset:64
	v_add_u32_e32 v8, 0xff, v3
	v_cmp_lt_u32_e32 vcc, s18, v8
	s_and_b64 s[14:15], s[12:13], vcc
	s_andn2_b64 vcc, exec, s[14:15]
	s_cbranch_vccnz .LBB0_3342
	s_movk_i32 s14, 0x1ff
	v_cmp_lt_u32_e32 vcc, s14, v8
	v_lshrrev_b32_e32 v1, 8, v8
	v_mov_b32_e32 v5, 0
	s_cbranch_vccz .LBB0_3337
	v_lshrrev_b32_e32 v4, 6, v0
	v_and_b32_e32 v2, 0xfffffe, v1
	v_lshl_add_u64 v[4:5], s[8:9], 0, v[4:5]
	s_mov_b64 s[14:15], 0x3000
	v_mov_b32_e32 v6, 16
	v_lshl_add_u64 v[4:5], v[4:5], 0, s[14:15]
	v_mov_b32_e32 v7, v6
	v_mov_b32_e32 v3, v2

.LBB0_3342:
	v_mov_b32_e32 v3, 0x1000
	v_mov_b32_e32 v4, v117
	v_and_b32_e32 v2, 0xffffff00, v8
	v_mov_b32_e32 v1, 0
	v_add_u32_e32 v2, v2, v0
	ds_write_b32 v1, v2 offset:68
	v_add_u32_e32 v11, 0xff, v4
	v_cmp_lt_u32_e32 vcc, s18, v11
	s_and_b64 s[14:15], s[12:13], vcc
	s_andn2_b64 vcc, exec, s[14:15]
	s_cbranch_vccnz .LBB0_3352
	s_movk_i32 s14, 0x1ff
	v_cmp_lt_u32_e32 vcc, s14, v11
	v_lshrrev_b32_e32 v5, 8, v11
	s_cbranch_vccz .LBB0_3347
	v_lshrrev_b32_e32 v0, 6, v2
	v_and_b32_e32 v4, 0xfffffe, v5
	v_lshl_add_u64 v[6:7], s[8:9], 0, v[0:1]
	s_mov_b64 s[14:15], 0x3000
	v_mov_b32_e32 v8, 17
	v_lshl_add_u64 v[6:7], v[6:7], 0, s[14:15]
	v_mov_b32_e32 v9, v8
	v_mov_b32_e32 v0, v4

.LBB0_3352:
	v_mov_b32_e32 v3, v118
	s_movk_i32 s18, 0xff
	v_and_b32_e32 v0, 0xffffff00, v11
	v_add_u32_e32 v0, v0, v2
	ds_write_b32 v1, v0 offset:72
	v_add_u32_e32 v8, 0xff, v3
	v_cmp_lt_u32_e32 vcc, s18, v8
	s_and_b64 s[14:15], s[12:13], vcc
	s_andn2_b64 vcc, exec, s[14:15]
	s_cbranch_vccnz .LBB0_3362
	s_movk_i32 s14, 0x1ff
	v_cmp_lt_u32_e32 vcc, s14, v8
	v_lshrrev_b32_e32 v1, 8, v8
	v_mov_b32_e32 v5, 0
	s_cbranch_vccz .LBB0_3357
	v_lshrrev_b32_e32 v4, 6, v0
	v_and_b32_e32 v2, 0xfffffe, v1
	v_lshl_add_u64 v[4:5], s[8:9], 0, v[4:5]
	s_mov_b64 s[14:15], 0x3000
	v_mov_b32_e32 v6, 18
	v_lshl_add_u64 v[4:5], v[4:5], 0, s[14:15]
	v_mov_b32_e32 v7, v6
	v_mov_b32_e32 v3, v2

.LBB0_3362:
	v_mov_b32_e32 v3, 0x1000
	v_mov_b32_e32 v4, v119
	v_and_b32_e32 v2, 0xffffff00, v8
	v_mov_b32_e32 v1, 0
	v_add_u32_e32 v2, v2, v0
	ds_write_b32 v1, v2 offset:76
	s_waitcnt vmcnt(0)
	v_add_u32_e32 v11, 0xff, v4
	v_cmp_lt_u32_e32 vcc, s18, v11
	s_and_b64 s[14:15], s[12:13], vcc
	s_andn2_b64 vcc, exec, s[14:15]
	s_cbranch_vccnz .LBB0_3372
	s_movk_i32 s14, 0x1ff
	v_cmp_lt_u32_e32 vcc, s14, v11
	v_lshrrev_b32_e32 v5, 8, v11
	s_cbranch_vccz .LBB0_3367
	v_lshrrev_b32_e32 v0, 6, v2
	v_and_b32_e32 v4, 0xfffffe, v5
	v_lshl_add_u64 v[6:7], s[8:9], 0, v[0:1]
	s_mov_b64 s[14:15], 0x3000
	v_mov_b32_e32 v8, 19
	v_lshl_add_u64 v[6:7], v[6:7], 0, s[14:15]
	v_mov_b32_e32 v9, v8
	v_mov_b32_e32 v0, v4

.LBB0_3372:
	v_mov_b32_e32 v3, v120
	s_movk_i32 s18, 0xff
	v_and_b32_e32 v0, 0xffffff00, v11
	v_add_u32_e32 v0, v0, v2
	ds_write_b32 v1, v0 offset:80
	v_add_u32_e32 v8, 0xff, v3
	v_cmp_lt_u32_e32 vcc, s18, v8
	s_and_b64 s[14:15], s[12:13], vcc
	s_andn2_b64 vcc, exec, s[14:15]
	s_cbranch_vccnz .LBB0_3382
	s_movk_i32 s14, 0x1ff
	v_cmp_lt_u32_e32 vcc, s14, v8
	v_lshrrev_b32_e32 v1, 8, v8
	v_mov_b32_e32 v5, 0
	s_cbranch_vccz .LBB0_3377
	v_lshrrev_b32_e32 v4, 6, v0
	v_and_b32_e32 v2, 0xfffffe, v1
	v_lshl_add_u64 v[4:5], s[8:9], 0, v[4:5]
	s_mov_b64 s[14:15], 0x3000
	v_mov_b32_e32 v6, 20
	v_lshl_add_u64 v[4:5], v[4:5], 0, s[14:15]
	v_mov_b32_e32 v7, v6
	v_mov_b32_e32 v3, v2

.LBB0_3382:
	v_mov_b32_e32 v3, 0x1000
	v_mov_b32_e32 v4, v121
	v_and_b32_e32 v2, 0xffffff00, v8
	v_mov_b32_e32 v1, 0
	v_add_u32_e32 v2, v2, v0
	ds_write_b32 v1, v2 offset:84
	v_add_u32_e32 v11, 0xff, v4
	v_cmp_lt_u32_e32 vcc, s18, v11
	s_and_b64 s[14:15], s[12:13], vcc
	s_andn2_b64 vcc, exec, s[14:15]
	s_cbranch_vccnz .LBB0_3392
	s_movk_i32 s14, 0x1ff
	v_cmp_lt_u32_e32 vcc, s14, v11
	v_lshrrev_b32_e32 v5, 8, v11
	s_cbranch_vccz .LBB0_3387
	v_lshrrev_b32_e32 v0, 6, v2
	v_and_b32_e32 v4, 0xfffffe, v5
	v_lshl_add_u64 v[6:7], s[8:9], 0, v[0:1]
	s_mov_b64 s[14:15], 0x3000
	v_mov_b32_e32 v8, 21
	v_lshl_add_u64 v[6:7], v[6:7], 0, s[14:15]
	v_mov_b32_e32 v9, v8
	v_mov_b32_e32 v0, v4

.LBB0_3392:
	v_mov_b32_e32 v3, v122
	s_movk_i32 s18, 0xff
	v_and_b32_e32 v0, 0xffffff00, v11
	v_add_u32_e32 v0, v0, v2
	ds_write_b32 v1, v0 offset:88
	v_add_u32_e32 v8, 0xff, v3
	v_cmp_lt_u32_e32 vcc, s18, v8
	s_and_b64 s[14:15], s[12:13], vcc
	s_andn2_b64 vcc, exec, s[14:15]
	s_cbranch_vccnz .LBB0_3402
	s_movk_i32 s14, 0x1ff
	v_cmp_lt_u32_e32 vcc, s14, v8
	v_lshrrev_b32_e32 v1, 8, v8
	v_mov_b32_e32 v5, 0
	s_cbranch_vccz .LBB0_3397
	v_lshrrev_b32_e32 v4, 6, v0
	v_and_b32_e32 v2, 0xfffffe, v1
	v_lshl_add_u64 v[4:5], s[8:9], 0, v[4:5]
	s_mov_b64 s[14:15], 0x3000
	v_mov_b32_e32 v6, 22
	v_lshl_add_u64 v[4:5], v[4:5], 0, s[14:15]
	v_mov_b32_e32 v7, v6
	v_mov_b32_e32 v3, v2

.LBB0_3402:
	v_mov_b32_e32 v3, 0x1000
	v_mov_b32_e32 v4, v123
	v_and_b32_e32 v2, 0xffffff00, v8
	v_mov_b32_e32 v1, 0
	v_add_u32_e32 v2, v2, v0
	ds_write_b32 v1, v2 offset:92
	s_waitcnt vmcnt(0)
	v_add_u32_e32 v11, 0xff, v4
	v_cmp_lt_u32_e32 vcc, s18, v11
	s_and_b64 s[14:15], s[12:13], vcc
	s_andn2_b64 vcc, exec, s[14:15]
	s_cbranch_vccnz .LBB0_3412
	s_movk_i32 s14, 0x1ff
	v_cmp_lt_u32_e32 vcc, s14, v11
	v_lshrrev_b32_e32 v5, 8, v11
	s_cbranch_vccz .LBB0_3407
	v_lshrrev_b32_e32 v0, 6, v2
	v_and_b32_e32 v4, 0xfffffe, v5
	v_lshl_add_u64 v[6:7], s[8:9], 0, v[0:1]
	s_mov_b64 s[14:15], 0x3000
	v_mov_b32_e32 v8, 23
	v_lshl_add_u64 v[6:7], v[6:7], 0, s[14:15]
	v_mov_b32_e32 v9, v8
	v_mov_b32_e32 v0, v4

.LBB0_3412:
	v_mov_b32_e32 v3, v124
	s_movk_i32 s18, 0xff
	v_and_b32_e32 v0, 0xffffff00, v11
	v_add_u32_e32 v0, v0, v2
	ds_write_b32 v1, v0 offset:96
	v_add_u32_e32 v8, 0xff, v3
	v_cmp_lt_u32_e32 vcc, s18, v8
	s_and_b64 s[14:15], s[12:13], vcc
	s_andn2_b64 vcc, exec, s[14:15]
	s_cbranch_vccnz .LBB0_3422
	s_movk_i32 s14, 0x1ff
	v_cmp_lt_u32_e32 vcc, s14, v8
	v_lshrrev_b32_e32 v1, 8, v8
	v_mov_b32_e32 v5, 0
	s_cbranch_vccz .LBB0_3417
	v_lshrrev_b32_e32 v4, 6, v0
	v_and_b32_e32 v2, 0xfffffe, v1
	v_lshl_add_u64 v[4:5], s[8:9], 0, v[4:5]
	s_mov_b64 s[14:15], 0x3000
	v_mov_b32_e32 v6, 24
	v_lshl_add_u64 v[4:5], v[4:5], 0, s[14:15]
	v_mov_b32_e32 v7, v6
	v_mov_b32_e32 v3, v2

.LBB0_3422:
	v_mov_b32_e32 v3, 0x1000
	v_mov_b32_e32 v4, v125
	v_and_b32_e32 v2, 0xffffff00, v8
	v_mov_b32_e32 v1, 0
	v_add_u32_e32 v2, v2, v0
	ds_write_b32 v1, v2 offset:100
	v_add_u32_e32 v11, 0xff, v4
	v_cmp_lt_u32_e32 vcc, s18, v11
	s_and_b64 s[14:15], s[12:13], vcc
	s_andn2_b64 vcc, exec, s[14:15]
	s_cbranch_vccnz .LBB0_3432
	s_movk_i32 s14, 0x1ff
	v_cmp_lt_u32_e32 vcc, s14, v11
	v_lshrrev_b32_e32 v5, 8, v11
	s_cbranch_vccz .LBB0_3427
	v_lshrrev_b32_e32 v0, 6, v2
	v_and_b32_e32 v4, 0xfffffe, v5
	v_lshl_add_u64 v[6:7], s[8:9], 0, v[0:1]
	s_mov_b64 s[14:15], 0x3000
	v_mov_b32_e32 v8, 25
	v_lshl_add_u64 v[6:7], v[6:7], 0, s[14:15]
	v_mov_b32_e32 v9, v8
	v_mov_b32_e32 v0, v4

.LBB0_3432:
	v_mov_b32_e32 v3, v126
	s_movk_i32 s18, 0xff
	v_and_b32_e32 v0, 0xffffff00, v11
	v_add_u32_e32 v0, v0, v2
	ds_write_b32 v1, v0 offset:104
	v_add_u32_e32 v8, 0xff, v3
	v_cmp_lt_u32_e32 vcc, s18, v8
	s_and_b64 s[14:15], s[12:13], vcc
	s_andn2_b64 vcc, exec, s[14:15]
	s_cbranch_vccnz .LBB0_3442
	s_movk_i32 s14, 0x1ff
	v_cmp_lt_u32_e32 vcc, s14, v8
	v_lshrrev_b32_e32 v1, 8, v8
	v_mov_b32_e32 v5, 0
	s_cbranch_vccz .LBB0_3437
	v_lshrrev_b32_e32 v4, 6, v0
	v_and_b32_e32 v2, 0xfffffe, v1
	v_lshl_add_u64 v[4:5], s[8:9], 0, v[4:5]
	s_mov_b64 s[14:15], 0x3000
	v_mov_b32_e32 v6, 26
	v_lshl_add_u64 v[4:5], v[4:5], 0, s[14:15]
	v_mov_b32_e32 v7, v6
	v_mov_b32_e32 v3, v2

.LBB0_3442:
	v_mov_b32_e32 v3, 0x1000
	v_mov_b32_e32 v4, v127
	v_and_b32_e32 v2, 0xffffff00, v8
	v_mov_b32_e32 v1, 0
	v_add_u32_e32 v2, v2, v0
	ds_write_b32 v1, v2 offset:108
	s_waitcnt vmcnt(0)
	v_add_u32_e32 v11, 0xff, v4
	v_cmp_lt_u32_e32 vcc, s18, v11
	s_and_b64 s[14:15], s[12:13], vcc
	s_andn2_b64 vcc, exec, s[14:15]
	s_cbranch_vccnz .LBB0_3452
	s_movk_i32 s14, 0x1ff
	v_cmp_lt_u32_e32 vcc, s14, v11
	v_lshrrev_b32_e32 v5, 8, v11
	s_cbranch_vccz .LBB0_3447
	v_lshrrev_b32_e32 v0, 6, v2
	v_and_b32_e32 v4, 0xfffffe, v5
	v_lshl_add_u64 v[6:7], s[8:9], 0, v[0:1]
	s_mov_b64 s[14:15], 0x3000
	v_mov_b32_e32 v8, 27
	v_lshl_add_u64 v[6:7], v[6:7], 0, s[14:15]
	v_mov_b32_e32 v9, v8
	v_mov_b32_e32 v0, v4

.LBB0_3452:
	v_mov_b32_e32 v3, v128
	s_movk_i32 s18, 0xff
	v_and_b32_e32 v0, 0xffffff00, v11
	v_add_u32_e32 v0, v0, v2
	ds_write_b32 v1, v0 offset:112
	v_add_u32_e32 v8, 0xff, v3
	v_cmp_lt_u32_e32 vcc, s18, v8
	s_and_b64 s[14:15], s[12:13], vcc
	s_andn2_b64 vcc, exec, s[14:15]
	s_cbranch_vccnz .LBB0_3462
	s_movk_i32 s14, 0x1ff
	v_cmp_lt_u32_e32 vcc, s14, v8
	v_lshrrev_b32_e32 v1, 8, v8
	v_mov_b32_e32 v5, 0
	s_cbranch_vccz .LBB0_3457
	v_lshrrev_b32_e32 v4, 6, v0
	v_and_b32_e32 v2, 0xfffffe, v1
	v_lshl_add_u64 v[4:5], s[8:9], 0, v[4:5]
	s_mov_b64 s[14:15], 0x3000
	v_mov_b32_e32 v6, 28
	v_lshl_add_u64 v[4:5], v[4:5], 0, s[14:15]
	v_mov_b32_e32 v7, v6
	v_mov_b32_e32 v3, v2

.LBB0_3462:
	v_mov_b32_e32 v3, 0x1000
	v_mov_b32_e32 v4, v129
	v_and_b32_e32 v2, 0xffffff00, v8
	v_mov_b32_e32 v1, 0
	v_add_u32_e32 v2, v2, v0
	ds_write_b32 v1, v2 offset:116
	v_add_u32_e32 v11, 0xff, v4
	v_cmp_lt_u32_e32 vcc, s18, v11
	s_and_b64 s[14:15], s[12:13], vcc
	s_andn2_b64 vcc, exec, s[14:15]
	s_cbranch_vccnz .LBB0_3472
	s_movk_i32 s14, 0x1ff
	v_cmp_lt_u32_e32 vcc, s14, v11
	v_lshrrev_b32_e32 v5, 8, v11
	s_cbranch_vccz .LBB0_3467
	v_lshrrev_b32_e32 v0, 6, v2
	v_and_b32_e32 v4, 0xfffffe, v5
	v_lshl_add_u64 v[6:7], s[8:9], 0, v[0:1]
	s_mov_b64 s[14:15], 0x3000
	v_mov_b32_e32 v8, 29
	v_lshl_add_u64 v[6:7], v[6:7], 0, s[14:15]
	v_mov_b32_e32 v9, v8
	v_mov_b32_e32 v0, v4

.LBB0_3472:
	v_mov_b32_e32 v3, v130
	s_movk_i32 s18, 0xff
	v_and_b32_e32 v0, 0xffffff00, v11
	v_add_u32_e32 v0, v0, v2
	ds_write_b32 v1, v0 offset:120
	v_add_u32_e32 v8, 0xff, v3
	v_cmp_lt_u32_e32 vcc, s18, v8
	s_and_b64 s[14:15], s[12:13], vcc
	s_andn2_b64 vcc, exec, s[14:15]
	s_cbranch_vccnz .LBB0_3482
	s_movk_i32 s14, 0x1ff
	v_cmp_lt_u32_e32 vcc, s14, v8
	v_lshrrev_b32_e32 v1, 8, v8
	v_mov_b32_e32 v5, 0
	s_cbranch_vccz .LBB0_3477
	v_lshrrev_b32_e32 v4, 6, v0
	v_and_b32_e32 v2, 0xfffffe, v1
	v_lshl_add_u64 v[4:5], s[8:9], 0, v[4:5]
	s_mov_b64 s[14:15], 0x3000
	v_mov_b32_e32 v6, 30
	v_lshl_add_u64 v[4:5], v[4:5], 0, s[14:15]
	v_mov_b32_e32 v7, v6
	v_mov_b32_e32 v3, v2

.LBB0_3482:
	v_mov_b32_e32 v1, 0x1000
	v_mov_b32_e32 v1, v131
	v_and_b32_e32 v2, 0xffffff00, v8
	v_mov_b32_e32 v5, 0
	v_add_u32_e32 v0, v2, v0
	ds_write_b32 v5, v0 offset:124
	s_waitcnt vmcnt(0)
	v_add_u32_e32 v1, 0xff, v1
	v_cmp_lt_u32_e32 vcc, s18, v1
	s_and_b64 s[14:15], s[12:13], vcc
	s_andn2_b64 vcc, exec, s[14:15]
	s_cbranch_vccnz .LBB0_3492
	s_movk_i32 s14, 0x1ff
	v_cmp_lt_u32_e32 vcc, s14, v1
	v_lshrrev_b32_e32 v3, 8, v1
	s_cbranch_vccz .LBB0_3487
	v_lshrrev_b32_e32 v4, 6, v0
	v_and_b32_e32 v2, 0xfffffe, v3
	v_lshl_add_u64 v[4:5], s[8:9], 0, v[4:5]
	s_mov_b64 s[14:15], 0x3000
	v_mov_b32_e32 v6, 31
	v_lshl_add_u64 v[4:5], v[4:5], 0, s[14:15]
	v_mov_b32_e32 v7, v6
	v_mov_b32_e32 v8, v2
